# proA GEMV rewritten: shared silu table in LDS + 48-deep w prefetch (plus router/conv wait fixes)
# speedup vs baseline: 1.0110x; 1.0092x over previous
.LBB0_11:
	s_mul_hi_i32 s16, s20, 0x2aaaaaab
	s_ashr_i32 s17, s16, 4
	s_lshr_b32 s23, s16, 31
	s_add_i32 s17, s17, s23
	s_mul_i32 s22, s17, 0x60
	s_sub_i32 s24, s20, s22
	s_lshr_b32 s22, s17, 29
	s_add_i32 s22, s17, s22
	s_and_b32 s22, s22, -8
	s_sub_i32 s22, s17, s22
	s_ashr_i32 s16, s16, 7
	s_add_i32 s23, s16, s23
	s_lshl_b32 s16, s22, 7
	s_ashr_i32 s17, s16, 31
	s_lshl_b64 s[26:27], s[16:17], 2
	v_lshl_or_b32 v4, s24, 6, v13
	s_add_u32 s24, s8, s26
	s_addc_u32 s25, s9, s27
	s_add_u32 s26, s6, s26
	s_addc_u32 s27, s7, s27
	s_mul_i32 s28, s23, 0x1800000
	s_mul_i32 s29, s22, 0x300000
	s_mul_hi_i32 s17, s23, 0x1800000
	s_mul_hi_i32 s16, s16, 0x6000
	s_add_u32 s28, s28, s29
	s_addc_u32 s17, s17, s16
	s_add_u32 s16, s10, s28
	v_ashrrev_i32_e32 v5, 31, v4
	s_addc_u32 s17, s11, s17
	v_lshl_add_u64 v[10:11], v[4:5], 2, s[16:17]
	v_and_b32_e32 v22, 0x7f, v12
	v_lshrrev_b32_e32 v23, 7, v12
	v_lshlrev_b32_e32 v24, 2, v22
	v_lshl_add_u32 v25, v23, 12, v24
	v_add_u32_e32 v26, 0x4000, v25
	global_load_dword v27, v25, s[26:27]
	global_load_dword v28, v26, s[26:27]
	global_load_dword v29, v24, s[24:25]
	v_lshlrev_b32_e32 v30, 2, v4
	s_mov_b64 s[28:29], s[16:17]
	global_load_dword v32, v30, s[28:29]
	s_add_u32 s28, s28, 0x6000
	s_addc_u32 s29, s29, 0
	global_load_dword v33, v30, s[28:29]
	s_add_u32 s28, s28, 0x6000
	s_addc_u32 s29, s29, 0
	global_load_dword v34, v30, s[28:29]
	s_add_u32 s28, s28, 0x6000
	s_addc_u32 s29, s29, 0
	global_load_dword v35, v30, s[28:29]
	s_add_u32 s28, s28, 0x6000
	s_addc_u32 s29, s29, 0
	global_load_dword v36, v30, s[28:29]
	s_add_u32 s28, s28, 0x6000
	s_addc_u32 s29, s29, 0
	global_load_dword v37, v30, s[28:29]
	s_add_u32 s28, s28, 0x6000
	s_addc_u32 s29, s29, 0
	global_load_dword v38, v30, s[28:29]
	s_add_u32 s28, s28, 0x6000
	s_addc_u32 s29, s29, 0
	global_load_dword v39, v30, s[28:29]
	s_add_u32 s28, s28, 0x6000
	s_addc_u32 s29, s29, 0
	global_load_dword v40, v30, s[28:29]
	s_add_u32 s28, s28, 0x6000
	s_addc_u32 s29, s29, 0
	global_load_dword v41, v30, s[28:29]
	s_add_u32 s28, s28, 0x6000
	s_addc_u32 s29, s29, 0
	global_load_dword v42, v30, s[28:29]
	s_add_u32 s28, s28, 0x6000
	s_addc_u32 s29, s29, 0
	global_load_dword v43, v30, s[28:29]
	s_add_u32 s28, s28, 0x6000
	s_addc_u32 s29, s29, 0
	global_load_dword v44, v30, s[28:29]
	s_add_u32 s28, s28, 0x6000
	s_addc_u32 s29, s29, 0
	global_load_dword v45, v30, s[28:29]
	s_add_u32 s28, s28, 0x6000
	s_addc_u32 s29, s29, 0
	global_load_dword v46, v30, s[28:29]
	s_add_u32 s28, s28, 0x6000
	s_addc_u32 s29, s29, 0
	global_load_dword v47, v30, s[28:29]
	s_add_u32 s28, s28, 0x6000
	s_addc_u32 s29, s29, 0
	global_load_dword v48, v30, s[28:29]
	s_add_u32 s28, s28, 0x6000
	s_addc_u32 s29, s29, 0
	global_load_dword v49, v30, s[28:29]
	s_add_u32 s28, s28, 0x6000
	s_addc_u32 s29, s29, 0
	global_load_dword v50, v30, s[28:29]
	s_add_u32 s28, s28, 0x6000
	s_addc_u32 s29, s29, 0
	global_load_dword v51, v30, s[28:29]
	s_add_u32 s28, s28, 0x6000
	s_addc_u32 s29, s29, 0
	global_load_dword v52, v30, s[28:29]
	s_add_u32 s28, s28, 0x6000
	s_addc_u32 s29, s29, 0
	global_load_dword v53, v30, s[28:29]
	s_add_u32 s28, s28, 0x6000
	s_addc_u32 s29, s29, 0
	global_load_dword v54, v30, s[28:29]
	s_add_u32 s28, s28, 0x6000
	s_addc_u32 s29, s29, 0
	global_load_dword v55, v30, s[28:29]
	s_add_u32 s28, s28, 0x6000
	s_addc_u32 s29, s29, 0
	global_load_dword v56, v30, s[28:29]
	s_add_u32 s28, s28, 0x6000
	s_addc_u32 s29, s29, 0
	global_load_dword v57, v30, s[28:29]
	s_add_u32 s28, s28, 0x6000
	s_addc_u32 s29, s29, 0
	global_load_dword v58, v30, s[28:29]
	s_add_u32 s28, s28, 0x6000
	s_addc_u32 s29, s29, 0
	global_load_dword v59, v30, s[28:29]
	s_add_u32 s28, s28, 0x6000
	s_addc_u32 s29, s29, 0
	global_load_dword v60, v30, s[28:29]
	s_add_u32 s28, s28, 0x6000
	s_addc_u32 s29, s29, 0
	global_load_dword v61, v30, s[28:29]
	s_add_u32 s28, s28, 0x6000
	s_addc_u32 s29, s29, 0
	global_load_dword v62, v30, s[28:29]
	s_add_u32 s28, s28, 0x6000
	s_addc_u32 s29, s29, 0
	global_load_dword v63, v30, s[28:29]
	s_add_u32 s28, s28, 0x6000
	s_addc_u32 s29, s29, 0
	global_load_dword v64, v30, s[28:29]
	s_add_u32 s28, s28, 0x6000
	s_addc_u32 s29, s29, 0
	global_load_dword v65, v30, s[28:29]
	s_add_u32 s28, s28, 0x6000
	s_addc_u32 s29, s29, 0
	global_load_dword v66, v30, s[28:29]
	s_add_u32 s28, s28, 0x6000
	s_addc_u32 s29, s29, 0
	global_load_dword v67, v30, s[28:29]
	s_add_u32 s28, s28, 0x6000
	s_addc_u32 s29, s29, 0
	global_load_dword v68, v30, s[28:29]
	s_add_u32 s28, s28, 0x6000
	s_addc_u32 s29, s29, 0
	global_load_dword v69, v30, s[28:29]
	s_add_u32 s28, s28, 0x6000
	s_addc_u32 s29, s29, 0
	global_load_dword v70, v30, s[28:29]
	s_add_u32 s28, s28, 0x6000
	s_addc_u32 s29, s29, 0
	global_load_dword v71, v30, s[28:29]
	s_add_u32 s28, s28, 0x6000
	s_addc_u32 s29, s29, 0
	global_load_dword v72, v30, s[28:29]
	s_add_u32 s28, s28, 0x6000
	s_addc_u32 s29, s29, 0
	global_load_dword v73, v30, s[28:29]
	s_add_u32 s28, s28, 0x6000
	s_addc_u32 s29, s29, 0
	global_load_dword v74, v30, s[28:29]
	s_add_u32 s28, s28, 0x6000
	s_addc_u32 s29, s29, 0
	global_load_dword v75, v30, s[28:29]
	s_add_u32 s28, s28, 0x6000
	s_addc_u32 s29, s29, 0
	global_load_dword v76, v30, s[28:29]
	s_add_u32 s28, s28, 0x6000
	s_addc_u32 s29, s29, 0
	global_load_dword v77, v30, s[28:29]
	s_add_u32 s28, s28, 0x6000
	s_addc_u32 s29, s29, 0
	global_load_dword v78, v30, s[28:29]
	s_add_u32 s28, s28, 0x6000
	s_addc_u32 s29, s29, 0
	global_load_dword v79, v30, s[28:29]
	s_add_u32 s28, s28, 0x6000
	s_addc_u32 s29, s29, 0
	s_waitcnt vmcnt(48)
	v_mul_f32_e32 v200, 0xbfb8aa3b, v27
	v_mul_f32_e32 v201, 0xbfb8aa3b, v28
	v_mul_f32_e32 v202, 0xbfb8aa3b, v29
	v_exp_f32_e32 v200, v200
	v_exp_f32_e32 v201, v201
	v_exp_f32_e32 v202, v202
	s_nop 0
	v_add_f32_e32 v200, 1.0, v200
	v_add_f32_e32 v201, 1.0, v201
	v_add_f32_e32 v202, 1.0, v202
	v_rcp_f32_e32 v200, v200
	v_rcp_f32_e32 v201, v201
	v_rcp_f32_e32 v202, v202
	s_nop 0
	v_mul_f32_e32 v27, v27, v200
	v_mul_f32_e32 v28, v28, v201
	v_mul_f32_e32 v29, v29, v202
	v_lshlrev_b32_e32 v31, 6, v22
	v_lshl_add_u32 v203, v23, 2, v31
	ds_write_b32 v203, v27
	ds_write_b32 v203, v28 offset:16
	ds_write_b32 v31, v29 offset:32
	s_waitcnt lgkmcnt(0)
	s_barrier
	v_mov_b32_e32 v0, 0
	v_mov_b32_e32 v1, 0
	v_mov_b32_e32 v2, 0
	v_mov_b32_e32 v3, 0
	v_mov_b32_e32 v4, 0
	v_mov_b32_e32 v5, 0
	v_mov_b32_e32 v6, 0
	v_mov_b32_e32 v7, 0
	v_mov_b32_e32 v8, 0
	v_mov_b32_e32 v9, 0
	ds_read_b128 v[96:99], v9 offset:0
	ds_read_b128 v[100:103], v9 offset:16
	ds_read_b32 v104, v9 offset:32
	ds_read_b128 v[108:111], v9 offset:64
	ds_read_b128 v[112:115], v9 offset:80
	ds_read_b32 v116, v9 offset:96
	s_waitcnt vmcnt(32)
	global_load_dword v80, v30, s[28:29]
	s_add_u32 s28, s28, 0x6000
	s_addc_u32 s29, s29, 0
	global_load_dword v81, v30, s[28:29]
	s_add_u32 s28, s28, 0x6000
	s_addc_u32 s29, s29, 0
	global_load_dword v82, v30, s[28:29]
	s_add_u32 s28, s28, 0x6000
	s_addc_u32 s29, s29, 0
	global_load_dword v83, v30, s[28:29]
	s_add_u32 s28, s28, 0x6000
	s_addc_u32 s29, s29, 0
	global_load_dword v84, v30, s[28:29]
	s_add_u32 s28, s28, 0x6000
	s_addc_u32 s29, s29, 0
	global_load_dword v85, v30, s[28:29]
	s_add_u32 s28, s28, 0x6000
	s_addc_u32 s29, s29, 0
	global_load_dword v86, v30, s[28:29]
	s_add_u32 s28, s28, 0x6000
	s_addc_u32 s29, s29, 0
	global_load_dword v87, v30, s[28:29]
	s_add_u32 s28, s28, 0x6000
	s_addc_u32 s29, s29, 0
	global_load_dword v88, v30, s[28:29]
	s_add_u32 s28, s28, 0x6000
	s_addc_u32 s29, s29, 0
	global_load_dword v89, v30, s[28:29]
	s_add_u32 s28, s28, 0x6000
	s_addc_u32 s29, s29, 0
	global_load_dword v90, v30, s[28:29]
	s_add_u32 s28, s28, 0x6000
	s_addc_u32 s29, s29, 0
	global_load_dword v91, v30, s[28:29]
	s_add_u32 s28, s28, 0x6000
	s_addc_u32 s29, s29, 0
	global_load_dword v92, v30, s[28:29]
	s_add_u32 s28, s28, 0x6000
	s_addc_u32 s29, s29, 0
	global_load_dword v93, v30, s[28:29]
	s_add_u32 s28, s28, 0x6000
	s_addc_u32 s29, s29, 0
	global_load_dword v94, v30, s[28:29]
	s_add_u32 s28, s28, 0x6000
	s_addc_u32 s29, s29, 0
	global_load_dword v95, v30, s[28:29]
	s_add_u32 s28, s28, 0x6000
	s_addc_u32 s29, s29, 0
	ds_read_b128 v[120:123], v9 offset:128
	ds_read_b128 v[124:127], v9 offset:144
	ds_read_b32 v128, v9 offset:160
	ds_read_b128 v[132:135], v9 offset:192
	ds_read_b128 v[136:139], v9 offset:208
	ds_read_b32 v140, v9 offset:224
	s_waitcnt lgkmcnt(6)
	v_fmac_f32_e32 v0, v32, v96
	v_fmac_f32_e32 v1, v32, v97
	v_fmac_f32_e32 v2, v32, v98
	v_fmac_f32_e32 v3, v32, v99
	v_fmac_f32_e32 v4, v32, v100
	v_fmac_f32_e32 v5, v32, v101
	v_fmac_f32_e32 v6, v32, v102
	v_fmac_f32_e32 v7, v32, v103
	v_fmac_f32_e32 v8, v32, v104
	v_fmac_f32_e32 v0, v33, v108
	v_fmac_f32_e32 v1, v33, v109
	v_fmac_f32_e32 v2, v33, v110
	v_fmac_f32_e32 v3, v33, v111
	v_fmac_f32_e32 v4, v33, v112
	v_fmac_f32_e32 v5, v33, v113
	v_fmac_f32_e32 v6, v33, v114
	v_fmac_f32_e32 v7, v33, v115
	v_fmac_f32_e32 v8, v33, v116
	ds_read_b128 v[96:99], v9 offset:256
	ds_read_b128 v[100:103], v9 offset:272
	ds_read_b32 v104, v9 offset:288
	ds_read_b128 v[108:111], v9 offset:320
	ds_read_b128 v[112:115], v9 offset:336
	ds_read_b32 v116, v9 offset:352
	s_waitcnt lgkmcnt(6)
	v_fmac_f32_e32 v0, v34, v120
	v_fmac_f32_e32 v1, v34, v121
	v_fmac_f32_e32 v2, v34, v122
	v_fmac_f32_e32 v3, v34, v123
	v_fmac_f32_e32 v4, v34, v124
	v_fmac_f32_e32 v5, v34, v125
	v_fmac_f32_e32 v6, v34, v126
	v_fmac_f32_e32 v7, v34, v127
	v_fmac_f32_e32 v8, v34, v128
	v_fmac_f32_e32 v0, v35, v132
	v_fmac_f32_e32 v1, v35, v133
	v_fmac_f32_e32 v2, v35, v134
	v_fmac_f32_e32 v3, v35, v135
	v_fmac_f32_e32 v4, v35, v136
	v_fmac_f32_e32 v5, v35, v137
	v_fmac_f32_e32 v6, v35, v138
	v_fmac_f32_e32 v7, v35, v139
	v_fmac_f32_e32 v8, v35, v140
	ds_read_b128 v[120:123], v9 offset:384
	ds_read_b128 v[124:127], v9 offset:400
	ds_read_b32 v128, v9 offset:416
	ds_read_b128 v[132:135], v9 offset:448
	ds_read_b128 v[136:139], v9 offset:464
	ds_read_b32 v140, v9 offset:480
	s_waitcnt lgkmcnt(6)
	v_fmac_f32_e32 v0, v36, v96
	v_fmac_f32_e32 v1, v36, v97
	v_fmac_f32_e32 v2, v36, v98
	v_fmac_f32_e32 v3, v36, v99
	v_fmac_f32_e32 v4, v36, v100
	v_fmac_f32_e32 v5, v36, v101
	v_fmac_f32_e32 v6, v36, v102
	v_fmac_f32_e32 v7, v36, v103
	v_fmac_f32_e32 v8, v36, v104
	v_fmac_f32_e32 v0, v37, v108
	v_fmac_f32_e32 v1, v37, v109
	v_fmac_f32_e32 v2, v37, v110
	v_fmac_f32_e32 v3, v37, v111
	v_fmac_f32_e32 v4, v37, v112
	v_fmac_f32_e32 v5, v37, v113
	v_fmac_f32_e32 v6, v37, v114
	v_fmac_f32_e32 v7, v37, v115
	v_fmac_f32_e32 v8, v37, v116
	ds_read_b128 v[96:99], v9 offset:512
	ds_read_b128 v[100:103], v9 offset:528
	ds_read_b32 v104, v9 offset:544
	ds_read_b128 v[108:111], v9 offset:576
	ds_read_b128 v[112:115], v9 offset:592
	ds_read_b32 v116, v9 offset:608
	s_waitcnt lgkmcnt(6)
	v_fmac_f32_e32 v0, v38, v120
	v_fmac_f32_e32 v1, v38, v121
	v_fmac_f32_e32 v2, v38, v122
	v_fmac_f32_e32 v3, v38, v123
	v_fmac_f32_e32 v4, v38, v124
	v_fmac_f32_e32 v5, v38, v125
	v_fmac_f32_e32 v6, v38, v126
	v_fmac_f32_e32 v7, v38, v127
	v_fmac_f32_e32 v8, v38, v128
	v_fmac_f32_e32 v0, v39, v132
	v_fmac_f32_e32 v1, v39, v133
	v_fmac_f32_e32 v2, v39, v134
	v_fmac_f32_e32 v3, v39, v135
	v_fmac_f32_e32 v4, v39, v136
	v_fmac_f32_e32 v5, v39, v137
	v_fmac_f32_e32 v6, v39, v138
	v_fmac_f32_e32 v7, v39, v139
	v_fmac_f32_e32 v8, v39, v140
	ds_read_b128 v[120:123], v9 offset:640
	ds_read_b128 v[124:127], v9 offset:656
	ds_read_b32 v128, v9 offset:672
	ds_read_b128 v[132:135], v9 offset:704
	ds_read_b128 v[136:139], v9 offset:720
	ds_read_b32 v140, v9 offset:736
	s_waitcnt lgkmcnt(6)
	v_fmac_f32_e32 v0, v40, v96
	v_fmac_f32_e32 v1, v40, v97
	v_fmac_f32_e32 v2, v40, v98
	v_fmac_f32_e32 v3, v40, v99
	v_fmac_f32_e32 v4, v40, v100
	v_fmac_f32_e32 v5, v40, v101
	v_fmac_f32_e32 v6, v40, v102
	v_fmac_f32_e32 v7, v40, v103
	v_fmac_f32_e32 v8, v40, v104
	v_fmac_f32_e32 v0, v41, v108
	v_fmac_f32_e32 v1, v41, v109
	v_fmac_f32_e32 v2, v41, v110
	v_fmac_f32_e32 v3, v41, v111
	v_fmac_f32_e32 v4, v41, v112
	v_fmac_f32_e32 v5, v41, v113
	v_fmac_f32_e32 v6, v41, v114
	v_fmac_f32_e32 v7, v41, v115
	v_fmac_f32_e32 v8, v41, v116
	ds_read_b128 v[96:99], v9 offset:768
	ds_read_b128 v[100:103], v9 offset:784
	ds_read_b32 v104, v9 offset:800
	ds_read_b128 v[108:111], v9 offset:832
	ds_read_b128 v[112:115], v9 offset:848
	ds_read_b32 v116, v9 offset:864
	s_waitcnt lgkmcnt(6)
	v_fmac_f32_e32 v0, v42, v120
	v_fmac_f32_e32 v1, v42, v121
	v_fmac_f32_e32 v2, v42, v122
	v_fmac_f32_e32 v3, v42, v123
	v_fmac_f32_e32 v4, v42, v124
	v_fmac_f32_e32 v5, v42, v125
	v_fmac_f32_e32 v6, v42, v126
	v_fmac_f32_e32 v7, v42, v127
	v_fmac_f32_e32 v8, v42, v128
	v_fmac_f32_e32 v0, v43, v132
	v_fmac_f32_e32 v1, v43, v133
	v_fmac_f32_e32 v2, v43, v134
	v_fmac_f32_e32 v3, v43, v135
	v_fmac_f32_e32 v4, v43, v136
	v_fmac_f32_e32 v5, v43, v137
	v_fmac_f32_e32 v6, v43, v138
	v_fmac_f32_e32 v7, v43, v139
	v_fmac_f32_e32 v8, v43, v140
	ds_read_b128 v[120:123], v9 offset:896
	ds_read_b128 v[124:127], v9 offset:912
	ds_read_b32 v128, v9 offset:928
	ds_read_b128 v[132:135], v9 offset:960
	ds_read_b128 v[136:139], v9 offset:976
	ds_read_b32 v140, v9 offset:992
	s_waitcnt lgkmcnt(6)
	v_fmac_f32_e32 v0, v44, v96
	v_fmac_f32_e32 v1, v44, v97
	v_fmac_f32_e32 v2, v44, v98
	v_fmac_f32_e32 v3, v44, v99
	v_fmac_f32_e32 v4, v44, v100
	v_fmac_f32_e32 v5, v44, v101
	v_fmac_f32_e32 v6, v44, v102
	v_fmac_f32_e32 v7, v44, v103
	v_fmac_f32_e32 v8, v44, v104
	v_fmac_f32_e32 v0, v45, v108
	v_fmac_f32_e32 v1, v45, v109
	v_fmac_f32_e32 v2, v45, v110
	v_fmac_f32_e32 v3, v45, v111
	v_fmac_f32_e32 v4, v45, v112
	v_fmac_f32_e32 v5, v45, v113
	v_fmac_f32_e32 v6, v45, v114
	v_fmac_f32_e32 v7, v45, v115
	v_fmac_f32_e32 v8, v45, v116
	ds_read_b128 v[96:99], v9 offset:1024
	ds_read_b128 v[100:103], v9 offset:1040
	ds_read_b32 v104, v9 offset:1056
	ds_read_b128 v[108:111], v9 offset:1088
	ds_read_b128 v[112:115], v9 offset:1104
	ds_read_b32 v116, v9 offset:1120
	s_waitcnt lgkmcnt(6)
	v_fmac_f32_e32 v0, v46, v120
	v_fmac_f32_e32 v1, v46, v121
	v_fmac_f32_e32 v2, v46, v122
	v_fmac_f32_e32 v3, v46, v123
	v_fmac_f32_e32 v4, v46, v124
	v_fmac_f32_e32 v5, v46, v125
	v_fmac_f32_e32 v6, v46, v126
	v_fmac_f32_e32 v7, v46, v127
	v_fmac_f32_e32 v8, v46, v128
	v_fmac_f32_e32 v0, v47, v132
	v_fmac_f32_e32 v1, v47, v133
	v_fmac_f32_e32 v2, v47, v134
	v_fmac_f32_e32 v3, v47, v135
	v_fmac_f32_e32 v4, v47, v136
	v_fmac_f32_e32 v5, v47, v137
	v_fmac_f32_e32 v6, v47, v138
	v_fmac_f32_e32 v7, v47, v139
	v_fmac_f32_e32 v8, v47, v140
	s_waitcnt vmcnt(32)
	global_load_dword v32, v30, s[28:29]
	s_add_u32 s28, s28, 0x6000
	s_addc_u32 s29, s29, 0
	global_load_dword v33, v30, s[28:29]
	s_add_u32 s28, s28, 0x6000
	s_addc_u32 s29, s29, 0
	global_load_dword v34, v30, s[28:29]
	s_add_u32 s28, s28, 0x6000
	s_addc_u32 s29, s29, 0
	global_load_dword v35, v30, s[28:29]
	s_add_u32 s28, s28, 0x6000
	s_addc_u32 s29, s29, 0
	global_load_dword v36, v30, s[28:29]
	s_add_u32 s28, s28, 0x6000
	s_addc_u32 s29, s29, 0
	global_load_dword v37, v30, s[28:29]
	s_add_u32 s28, s28, 0x6000
	s_addc_u32 s29, s29, 0
	global_load_dword v38, v30, s[28:29]
	s_add_u32 s28, s28, 0x6000
	s_addc_u32 s29, s29, 0
	global_load_dword v39, v30, s[28:29]
	s_add_u32 s28, s28, 0x6000
	s_addc_u32 s29, s29, 0
	global_load_dword v40, v30, s[28:29]
	s_add_u32 s28, s28, 0x6000
	s_addc_u32 s29, s29, 0
	global_load_dword v41, v30, s[28:29]
	s_add_u32 s28, s28, 0x6000
	s_addc_u32 s29, s29, 0
	global_load_dword v42, v30, s[28:29]
	s_add_u32 s28, s28, 0x6000
	s_addc_u32 s29, s29, 0
	global_load_dword v43, v30, s[28:29]
	s_add_u32 s28, s28, 0x6000
	s_addc_u32 s29, s29, 0
	global_load_dword v44, v30, s[28:29]
	s_add_u32 s28, s28, 0x6000
	s_addc_u32 s29, s29, 0
	global_load_dword v45, v30, s[28:29]
	s_add_u32 s28, s28, 0x6000
	s_addc_u32 s29, s29, 0
	global_load_dword v46, v30, s[28:29]
	s_add_u32 s28, s28, 0x6000
	s_addc_u32 s29, s29, 0
	global_load_dword v47, v30, s[28:29]
	s_add_u32 s28, s28, 0x6000
	s_addc_u32 s29, s29, 0
	ds_read_b128 v[120:123], v9 offset:1152
	ds_read_b128 v[124:127], v9 offset:1168
	ds_read_b32 v128, v9 offset:1184
	ds_read_b128 v[132:135], v9 offset:1216
	ds_read_b128 v[136:139], v9 offset:1232
	ds_read_b32 v140, v9 offset:1248
	s_waitcnt lgkmcnt(6)
	v_fmac_f32_e32 v0, v48, v96
	v_fmac_f32_e32 v1, v48, v97
	v_fmac_f32_e32 v2, v48, v98
	v_fmac_f32_e32 v3, v48, v99
	v_fmac_f32_e32 v4, v48, v100
	v_fmac_f32_e32 v5, v48, v101
	v_fmac_f32_e32 v6, v48, v102
	v_fmac_f32_e32 v7, v48, v103
	v_fmac_f32_e32 v8, v48, v104
	v_fmac_f32_e32 v0, v49, v108
	v_fmac_f32_e32 v1, v49, v109
	v_fmac_f32_e32 v2, v49, v110
	v_fmac_f32_e32 v3, v49, v111
	v_fmac_f32_e32 v4, v49, v112
	v_fmac_f32_e32 v5, v49, v113
	v_fmac_f32_e32 v6, v49, v114
	v_fmac_f32_e32 v7, v49, v115
	v_fmac_f32_e32 v8, v49, v116
	ds_read_b128 v[96:99], v9 offset:1280
	ds_read_b128 v[100:103], v9 offset:1296
	ds_read_b32 v104, v9 offset:1312
	ds_read_b128 v[108:111], v9 offset:1344
	ds_read_b128 v[112:115], v9 offset:1360
	ds_read_b32 v116, v9 offset:1376
	s_waitcnt lgkmcnt(6)
	v_fmac_f32_e32 v0, v50, v120
	v_fmac_f32_e32 v1, v50, v121
	v_fmac_f32_e32 v2, v50, v122
	v_fmac_f32_e32 v3, v50, v123
	v_fmac_f32_e32 v4, v50, v124
	v_fmac_f32_e32 v5, v50, v125
	v_fmac_f32_e32 v6, v50, v126
	v_fmac_f32_e32 v7, v50, v127
	v_fmac_f32_e32 v8, v50, v128
	v_fmac_f32_e32 v0, v51, v132
	v_fmac_f32_e32 v1, v51, v133
	v_fmac_f32_e32 v2, v51, v134
	v_fmac_f32_e32 v3, v51, v135
	v_fmac_f32_e32 v4, v51, v136
	v_fmac_f32_e32 v5, v51, v137
	v_fmac_f32_e32 v6, v51, v138
	v_fmac_f32_e32 v7, v51, v139
	v_fmac_f32_e32 v8, v51, v140
	ds_read_b128 v[120:123], v9 offset:1408
	ds_read_b128 v[124:127], v9 offset:1424
	ds_read_b32 v128, v9 offset:1440
	ds_read_b128 v[132:135], v9 offset:1472
	ds_read_b128 v[136:139], v9 offset:1488
	ds_read_b32 v140, v9 offset:1504
	s_waitcnt lgkmcnt(6)
	v_fmac_f32_e32 v0, v52, v96
	v_fmac_f32_e32 v1, v52, v97
	v_fmac_f32_e32 v2, v52, v98
	v_fmac_f32_e32 v3, v52, v99
	v_fmac_f32_e32 v4, v52, v100
	v_fmac_f32_e32 v5, v52, v101
	v_fmac_f32_e32 v6, v52, v102
	v_fmac_f32_e32 v7, v52, v103
	v_fmac_f32_e32 v8, v52, v104
	v_fmac_f32_e32 v0, v53, v108
	v_fmac_f32_e32 v1, v53, v109
	v_fmac_f32_e32 v2, v53, v110
	v_fmac_f32_e32 v3, v53, v111
	v_fmac_f32_e32 v4, v53, v112
	v_fmac_f32_e32 v5, v53, v113
	v_fmac_f32_e32 v6, v53, v114
	v_fmac_f32_e32 v7, v53, v115
	v_fmac_f32_e32 v8, v53, v116
	ds_read_b128 v[96:99], v9 offset:1536
	ds_read_b128 v[100:103], v9 offset:1552
	ds_read_b32 v104, v9 offset:1568
	ds_read_b128 v[108:111], v9 offset:1600
	ds_read_b128 v[112:115], v9 offset:1616
	ds_read_b32 v116, v9 offset:1632
	s_waitcnt lgkmcnt(6)
	v_fmac_f32_e32 v0, v54, v120
	v_fmac_f32_e32 v1, v54, v121
	v_fmac_f32_e32 v2, v54, v122
	v_fmac_f32_e32 v3, v54, v123
	v_fmac_f32_e32 v4, v54, v124
	v_fmac_f32_e32 v5, v54, v125
	v_fmac_f32_e32 v6, v54, v126
	v_fmac_f32_e32 v7, v54, v127
	v_fmac_f32_e32 v8, v54, v128
	v_fmac_f32_e32 v0, v55, v132
	v_fmac_f32_e32 v1, v55, v133
	v_fmac_f32_e32 v2, v55, v134
	v_fmac_f32_e32 v3, v55, v135
	v_fmac_f32_e32 v4, v55, v136
	v_fmac_f32_e32 v5, v55, v137
	v_fmac_f32_e32 v6, v55, v138
	v_fmac_f32_e32 v7, v55, v139
	v_fmac_f32_e32 v8, v55, v140
	ds_read_b128 v[120:123], v9 offset:1664
	ds_read_b128 v[124:127], v9 offset:1680
	ds_read_b32 v128, v9 offset:1696
	ds_read_b128 v[132:135], v9 offset:1728
	ds_read_b128 v[136:139], v9 offset:1744
	ds_read_b32 v140, v9 offset:1760
	s_waitcnt lgkmcnt(6)
	v_fmac_f32_e32 v0, v56, v96
	v_fmac_f32_e32 v1, v56, v97
	v_fmac_f32_e32 v2, v56, v98
	v_fmac_f32_e32 v3, v56, v99
	v_fmac_f32_e32 v4, v56, v100
	v_fmac_f32_e32 v5, v56, v101
	v_fmac_f32_e32 v6, v56, v102
	v_fmac_f32_e32 v7, v56, v103
	v_fmac_f32_e32 v8, v56, v104
	v_fmac_f32_e32 v0, v57, v108
	v_fmac_f32_e32 v1, v57, v109
	v_fmac_f32_e32 v2, v57, v110
	v_fmac_f32_e32 v3, v57, v111
	v_fmac_f32_e32 v4, v57, v112
	v_fmac_f32_e32 v5, v57, v113
	v_fmac_f32_e32 v6, v57, v114
	v_fmac_f32_e32 v7, v57, v115
	v_fmac_f32_e32 v8, v57, v116
	ds_read_b128 v[96:99], v9 offset:1792
	ds_read_b128 v[100:103], v9 offset:1808
	ds_read_b32 v104, v9 offset:1824
	ds_read_b128 v[108:111], v9 offset:1856
	ds_read_b128 v[112:115], v9 offset:1872
	ds_read_b32 v116, v9 offset:1888
	s_waitcnt lgkmcnt(6)
	v_fmac_f32_e32 v0, v58, v120
	v_fmac_f32_e32 v1, v58, v121
	v_fmac_f32_e32 v2, v58, v122
	v_fmac_f32_e32 v3, v58, v123
	v_fmac_f32_e32 v4, v58, v124
	v_fmac_f32_e32 v5, v58, v125
	v_fmac_f32_e32 v6, v58, v126
	v_fmac_f32_e32 v7, v58, v127
	v_fmac_f32_e32 v8, v58, v128
	v_fmac_f32_e32 v0, v59, v132
	v_fmac_f32_e32 v1, v59, v133
	v_fmac_f32_e32 v2, v59, v134
	v_fmac_f32_e32 v3, v59, v135
	v_fmac_f32_e32 v4, v59, v136
	v_fmac_f32_e32 v5, v59, v137
	v_fmac_f32_e32 v6, v59, v138
	v_fmac_f32_e32 v7, v59, v139
	v_fmac_f32_e32 v8, v59, v140
	ds_read_b128 v[120:123], v9 offset:1920
	ds_read_b128 v[124:127], v9 offset:1936
	ds_read_b32 v128, v9 offset:1952
	ds_read_b128 v[132:135], v9 offset:1984
	ds_read_b128 v[136:139], v9 offset:2000
	ds_read_b32 v140, v9 offset:2016
	s_waitcnt lgkmcnt(6)
	v_fmac_f32_e32 v0, v60, v96
	v_fmac_f32_e32 v1, v60, v97
	v_fmac_f32_e32 v2, v60, v98
	v_fmac_f32_e32 v3, v60, v99
	v_fmac_f32_e32 v4, v60, v100
	v_fmac_f32_e32 v5, v60, v101
	v_fmac_f32_e32 v6, v60, v102
	v_fmac_f32_e32 v7, v60, v103
	v_fmac_f32_e32 v8, v60, v104
	v_fmac_f32_e32 v0, v61, v108
	v_fmac_f32_e32 v1, v61, v109
	v_fmac_f32_e32 v2, v61, v110
	v_fmac_f32_e32 v3, v61, v111
	v_fmac_f32_e32 v4, v61, v112
	v_fmac_f32_e32 v5, v61, v113
	v_fmac_f32_e32 v6, v61, v114
	v_fmac_f32_e32 v7, v61, v115
	v_fmac_f32_e32 v8, v61, v116
	ds_read_b128 v[96:99], v9 offset:2048
	ds_read_b128 v[100:103], v9 offset:2064
	ds_read_b32 v104, v9 offset:2080
	ds_read_b128 v[108:111], v9 offset:2112
	ds_read_b128 v[112:115], v9 offset:2128
	ds_read_b32 v116, v9 offset:2144
	s_waitcnt lgkmcnt(6)
	v_fmac_f32_e32 v0, v62, v120
	v_fmac_f32_e32 v1, v62, v121
	v_fmac_f32_e32 v2, v62, v122
	v_fmac_f32_e32 v3, v62, v123
	v_fmac_f32_e32 v4, v62, v124
	v_fmac_f32_e32 v5, v62, v125
	v_fmac_f32_e32 v6, v62, v126
	v_fmac_f32_e32 v7, v62, v127
	v_fmac_f32_e32 v8, v62, v128
	v_fmac_f32_e32 v0, v63, v132
	v_fmac_f32_e32 v1, v63, v133
	v_fmac_f32_e32 v2, v63, v134
	v_fmac_f32_e32 v3, v63, v135
	v_fmac_f32_e32 v4, v63, v136
	v_fmac_f32_e32 v5, v63, v137
	v_fmac_f32_e32 v6, v63, v138
	v_fmac_f32_e32 v7, v63, v139
	v_fmac_f32_e32 v8, v63, v140
	s_waitcnt vmcnt(32)
	global_load_dword v48, v30, s[28:29]
	s_add_u32 s28, s28, 0x6000
	s_addc_u32 s29, s29, 0
	global_load_dword v49, v30, s[28:29]
	s_add_u32 s28, s28, 0x6000
	s_addc_u32 s29, s29, 0
	global_load_dword v50, v30, s[28:29]
	s_add_u32 s28, s28, 0x6000
	s_addc_u32 s29, s29, 0
	global_load_dword v51, v30, s[28:29]
	s_add_u32 s28, s28, 0x6000
	s_addc_u32 s29, s29, 0
	global_load_dword v52, v30, s[28:29]
	s_add_u32 s28, s28, 0x6000
	s_addc_u32 s29, s29, 0
	global_load_dword v53, v30, s[28:29]
	s_add_u32 s28, s28, 0x6000
	s_addc_u32 s29, s29, 0
	global_load_dword v54, v30, s[28:29]
	s_add_u32 s28, s28, 0x6000
	s_addc_u32 s29, s29, 0
	global_load_dword v55, v30, s[28:29]
	s_add_u32 s28, s28, 0x6000
	s_addc_u32 s29, s29, 0
	global_load_dword v56, v30, s[28:29]
	s_add_u32 s28, s28, 0x6000
	s_addc_u32 s29, s29, 0
	global_load_dword v57, v30, s[28:29]
	s_add_u32 s28, s28, 0x6000
	s_addc_u32 s29, s29, 0
	global_load_dword v58, v30, s[28:29]
	s_add_u32 s28, s28, 0x6000
	s_addc_u32 s29, s29, 0
	global_load_dword v59, v30, s[28:29]
	s_add_u32 s28, s28, 0x6000
	s_addc_u32 s29, s29, 0
	global_load_dword v60, v30, s[28:29]
	s_add_u32 s28, s28, 0x6000
	s_addc_u32 s29, s29, 0
	global_load_dword v61, v30, s[28:29]
	s_add_u32 s28, s28, 0x6000
	s_addc_u32 s29, s29, 0
	global_load_dword v62, v30, s[28:29]
	s_add_u32 s28, s28, 0x6000
	s_addc_u32 s29, s29, 0
	global_load_dword v63, v30, s[28:29]
	s_add_u32 s28, s28, 0x6000
	s_addc_u32 s29, s29, 0
	ds_read_b128 v[120:123], v9 offset:2176
	ds_read_b128 v[124:127], v9 offset:2192
	ds_read_b32 v128, v9 offset:2208
	ds_read_b128 v[132:135], v9 offset:2240
	ds_read_b128 v[136:139], v9 offset:2256
	ds_read_b32 v140, v9 offset:2272
	s_waitcnt lgkmcnt(6)
	v_fmac_f32_e32 v0, v64, v96
	v_fmac_f32_e32 v1, v64, v97
	v_fmac_f32_e32 v2, v64, v98
	v_fmac_f32_e32 v3, v64, v99
	v_fmac_f32_e32 v4, v64, v100
	v_fmac_f32_e32 v5, v64, v101
	v_fmac_f32_e32 v6, v64, v102
	v_fmac_f32_e32 v7, v64, v103
	v_fmac_f32_e32 v8, v64, v104
	v_fmac_f32_e32 v0, v65, v108
	v_fmac_f32_e32 v1, v65, v109
	v_fmac_f32_e32 v2, v65, v110
	v_fmac_f32_e32 v3, v65, v111
	v_fmac_f32_e32 v4, v65, v112
	v_fmac_f32_e32 v5, v65, v113
	v_fmac_f32_e32 v6, v65, v114
	v_fmac_f32_e32 v7, v65, v115
	v_fmac_f32_e32 v8, v65, v116
	ds_read_b128 v[96:99], v9 offset:2304
	ds_read_b128 v[100:103], v9 offset:2320
	ds_read_b32 v104, v9 offset:2336
	ds_read_b128 v[108:111], v9 offset:2368
	ds_read_b128 v[112:115], v9 offset:2384
	ds_read_b32 v116, v9 offset:2400
	s_waitcnt lgkmcnt(6)
	v_fmac_f32_e32 v0, v66, v120
	v_fmac_f32_e32 v1, v66, v121
	v_fmac_f32_e32 v2, v66, v122
	v_fmac_f32_e32 v3, v66, v123
	v_fmac_f32_e32 v4, v66, v124
	v_fmac_f32_e32 v5, v66, v125
	v_fmac_f32_e32 v6, v66, v126
	v_fmac_f32_e32 v7, v66, v127
	v_fmac_f32_e32 v8, v66, v128
	v_fmac_f32_e32 v0, v67, v132
	v_fmac_f32_e32 v1, v67, v133
	v_fmac_f32_e32 v2, v67, v134
	v_fmac_f32_e32 v3, v67, v135
	v_fmac_f32_e32 v4, v67, v136
	v_fmac_f32_e32 v5, v67, v137
	v_fmac_f32_e32 v6, v67, v138
	v_fmac_f32_e32 v7, v67, v139
	v_fmac_f32_e32 v8, v67, v140
	ds_read_b128 v[120:123], v9 offset:2432
	ds_read_b128 v[124:127], v9 offset:2448
	ds_read_b32 v128, v9 offset:2464
	ds_read_b128 v[132:135], v9 offset:2496
	ds_read_b128 v[136:139], v9 offset:2512
	ds_read_b32 v140, v9 offset:2528
	s_waitcnt lgkmcnt(6)
	v_fmac_f32_e32 v0, v68, v96
	v_fmac_f32_e32 v1, v68, v97
	v_fmac_f32_e32 v2, v68, v98
	v_fmac_f32_e32 v3, v68, v99
	v_fmac_f32_e32 v4, v68, v100
	v_fmac_f32_e32 v5, v68, v101
	v_fmac_f32_e32 v6, v68, v102
	v_fmac_f32_e32 v7, v68, v103
	v_fmac_f32_e32 v8, v68, v104
	v_fmac_f32_e32 v0, v69, v108
	v_fmac_f32_e32 v1, v69, v109
	v_fmac_f32_e32 v2, v69, v110
	v_fmac_f32_e32 v3, v69, v111
	v_fmac_f32_e32 v4, v69, v112
	v_fmac_f32_e32 v5, v69, v113
	v_fmac_f32_e32 v6, v69, v114
	v_fmac_f32_e32 v7, v69, v115
	v_fmac_f32_e32 v8, v69, v116
	ds_read_b128 v[96:99], v9 offset:2560
	ds_read_b128 v[100:103], v9 offset:2576
	ds_read_b32 v104, v9 offset:2592
	ds_read_b128 v[108:111], v9 offset:2624
	ds_read_b128 v[112:115], v9 offset:2640
	ds_read_b32 v116, v9 offset:2656
	s_waitcnt lgkmcnt(6)
	v_fmac_f32_e32 v0, v70, v120
	v_fmac_f32_e32 v1, v70, v121
	v_fmac_f32_e32 v2, v70, v122
	v_fmac_f32_e32 v3, v70, v123
	v_fmac_f32_e32 v4, v70, v124
	v_fmac_f32_e32 v5, v70, v125
	v_fmac_f32_e32 v6, v70, v126
	v_fmac_f32_e32 v7, v70, v127
	v_fmac_f32_e32 v8, v70, v128
	v_fmac_f32_e32 v0, v71, v132
	v_fmac_f32_e32 v1, v71, v133
	v_fmac_f32_e32 v2, v71, v134
	v_fmac_f32_e32 v3, v71, v135
	v_fmac_f32_e32 v4, v71, v136
	v_fmac_f32_e32 v5, v71, v137
	v_fmac_f32_e32 v6, v71, v138
	v_fmac_f32_e32 v7, v71, v139
	v_fmac_f32_e32 v8, v71, v140
	ds_read_b128 v[120:123], v9 offset:2688
	ds_read_b128 v[124:127], v9 offset:2704
	ds_read_b32 v128, v9 offset:2720
	ds_read_b128 v[132:135], v9 offset:2752
	ds_read_b128 v[136:139], v9 offset:2768
	ds_read_b32 v140, v9 offset:2784
	s_waitcnt lgkmcnt(6)
	v_fmac_f32_e32 v0, v72, v96
	v_fmac_f32_e32 v1, v72, v97
	v_fmac_f32_e32 v2, v72, v98
	v_fmac_f32_e32 v3, v72, v99
	v_fmac_f32_e32 v4, v72, v100
	v_fmac_f32_e32 v5, v72, v101
	v_fmac_f32_e32 v6, v72, v102
	v_fmac_f32_e32 v7, v72, v103
	v_fmac_f32_e32 v8, v72, v104
	v_fmac_f32_e32 v0, v73, v108
	v_fmac_f32_e32 v1, v73, v109
	v_fmac_f32_e32 v2, v73, v110
	v_fmac_f32_e32 v3, v73, v111
	v_fmac_f32_e32 v4, v73, v112
	v_fmac_f32_e32 v5, v73, v113
	v_fmac_f32_e32 v6, v73, v114
	v_fmac_f32_e32 v7, v73, v115
	v_fmac_f32_e32 v8, v73, v116
	ds_read_b128 v[96:99], v9 offset:2816
	ds_read_b128 v[100:103], v9 offset:2832
	ds_read_b32 v104, v9 offset:2848
	ds_read_b128 v[108:111], v9 offset:2880
	ds_read_b128 v[112:115], v9 offset:2896
	ds_read_b32 v116, v9 offset:2912
	s_waitcnt lgkmcnt(6)
	v_fmac_f32_e32 v0, v74, v120
	v_fmac_f32_e32 v1, v74, v121
	v_fmac_f32_e32 v2, v74, v122
	v_fmac_f32_e32 v3, v74, v123
	v_fmac_f32_e32 v4, v74, v124
	v_fmac_f32_e32 v5, v74, v125
	v_fmac_f32_e32 v6, v74, v126
	v_fmac_f32_e32 v7, v74, v127
	v_fmac_f32_e32 v8, v74, v128
	v_fmac_f32_e32 v0, v75, v132
	v_fmac_f32_e32 v1, v75, v133
	v_fmac_f32_e32 v2, v75, v134
	v_fmac_f32_e32 v3, v75, v135
	v_fmac_f32_e32 v4, v75, v136
	v_fmac_f32_e32 v5, v75, v137
	v_fmac_f32_e32 v6, v75, v138
	v_fmac_f32_e32 v7, v75, v139
	v_fmac_f32_e32 v8, v75, v140
	ds_read_b128 v[120:123], v9 offset:2944
	ds_read_b128 v[124:127], v9 offset:2960
	ds_read_b32 v128, v9 offset:2976
	ds_read_b128 v[132:135], v9 offset:3008
	ds_read_b128 v[136:139], v9 offset:3024
	ds_read_b32 v140, v9 offset:3040
	s_waitcnt lgkmcnt(6)
	v_fmac_f32_e32 v0, v76, v96
	v_fmac_f32_e32 v1, v76, v97
	v_fmac_f32_e32 v2, v76, v98
	v_fmac_f32_e32 v3, v76, v99
	v_fmac_f32_e32 v4, v76, v100
	v_fmac_f32_e32 v5, v76, v101
	v_fmac_f32_e32 v6, v76, v102
	v_fmac_f32_e32 v7, v76, v103
	v_fmac_f32_e32 v8, v76, v104
	v_fmac_f32_e32 v0, v77, v108
	v_fmac_f32_e32 v1, v77, v109
	v_fmac_f32_e32 v2, v77, v110
	v_fmac_f32_e32 v3, v77, v111
	v_fmac_f32_e32 v4, v77, v112
	v_fmac_f32_e32 v5, v77, v113
	v_fmac_f32_e32 v6, v77, v114
	v_fmac_f32_e32 v7, v77, v115
	v_fmac_f32_e32 v8, v77, v116
	ds_read_b128 v[96:99], v9 offset:3072
	ds_read_b128 v[100:103], v9 offset:3088
	ds_read_b32 v104, v9 offset:3104
	ds_read_b128 v[108:111], v9 offset:3136
	ds_read_b128 v[112:115], v9 offset:3152
	ds_read_b32 v116, v9 offset:3168
	s_waitcnt lgkmcnt(6)
	v_fmac_f32_e32 v0, v78, v120
	v_fmac_f32_e32 v1, v78, v121
	v_fmac_f32_e32 v2, v78, v122
	v_fmac_f32_e32 v3, v78, v123
	v_fmac_f32_e32 v4, v78, v124
	v_fmac_f32_e32 v5, v78, v125
	v_fmac_f32_e32 v6, v78, v126
	v_fmac_f32_e32 v7, v78, v127
	v_fmac_f32_e32 v8, v78, v128
	v_fmac_f32_e32 v0, v79, v132
	v_fmac_f32_e32 v1, v79, v133
	v_fmac_f32_e32 v2, v79, v134
	v_fmac_f32_e32 v3, v79, v135
	v_fmac_f32_e32 v4, v79, v136
	v_fmac_f32_e32 v5, v79, v137
	v_fmac_f32_e32 v6, v79, v138
	v_fmac_f32_e32 v7, v79, v139
	v_fmac_f32_e32 v8, v79, v140
	s_waitcnt vmcnt(32)
	global_load_dword v64, v30, s[28:29]
	s_add_u32 s28, s28, 0x6000
	s_addc_u32 s29, s29, 0
	global_load_dword v65, v30, s[28:29]
	s_add_u32 s28, s28, 0x6000
	s_addc_u32 s29, s29, 0
	global_load_dword v66, v30, s[28:29]
	s_add_u32 s28, s28, 0x6000
	s_addc_u32 s29, s29, 0
	global_load_dword v67, v30, s[28:29]
	s_add_u32 s28, s28, 0x6000
	s_addc_u32 s29, s29, 0
	global_load_dword v68, v30, s[28:29]
	s_add_u32 s28, s28, 0x6000
	s_addc_u32 s29, s29, 0
	global_load_dword v69, v30, s[28:29]
	s_add_u32 s28, s28, 0x6000
	s_addc_u32 s29, s29, 0
	global_load_dword v70, v30, s[28:29]
	s_add_u32 s28, s28, 0x6000
	s_addc_u32 s29, s29, 0
	global_load_dword v71, v30, s[28:29]
	s_add_u32 s28, s28, 0x6000
	s_addc_u32 s29, s29, 0
	global_load_dword v72, v30, s[28:29]
	s_add_u32 s28, s28, 0x6000
	s_addc_u32 s29, s29, 0
	global_load_dword v73, v30, s[28:29]
	s_add_u32 s28, s28, 0x6000
	s_addc_u32 s29, s29, 0
	global_load_dword v74, v30, s[28:29]
	s_add_u32 s28, s28, 0x6000
	s_addc_u32 s29, s29, 0
	global_load_dword v75, v30, s[28:29]
	s_add_u32 s28, s28, 0x6000
	s_addc_u32 s29, s29, 0
	global_load_dword v76, v30, s[28:29]
	s_add_u32 s28, s28, 0x6000
	s_addc_u32 s29, s29, 0
	global_load_dword v77, v30, s[28:29]
	s_add_u32 s28, s28, 0x6000
	s_addc_u32 s29, s29, 0
	global_load_dword v78, v30, s[28:29]
	s_add_u32 s28, s28, 0x6000
	s_addc_u32 s29, s29, 0
	global_load_dword v79, v30, s[28:29]
	s_add_u32 s28, s28, 0x6000
	s_addc_u32 s29, s29, 0
	ds_read_b128 v[120:123], v9 offset:3200
	ds_read_b128 v[124:127], v9 offset:3216
	ds_read_b32 v128, v9 offset:3232
	ds_read_b128 v[132:135], v9 offset:3264
	ds_read_b128 v[136:139], v9 offset:3280
	ds_read_b32 v140, v9 offset:3296
	s_waitcnt lgkmcnt(6)
	v_fmac_f32_e32 v0, v80, v96
	v_fmac_f32_e32 v1, v80, v97
	v_fmac_f32_e32 v2, v80, v98
	v_fmac_f32_e32 v3, v80, v99
	v_fmac_f32_e32 v4, v80, v100
	v_fmac_f32_e32 v5, v80, v101
	v_fmac_f32_e32 v6, v80, v102
	v_fmac_f32_e32 v7, v80, v103
	v_fmac_f32_e32 v8, v80, v104
	v_fmac_f32_e32 v0, v81, v108
	v_fmac_f32_e32 v1, v81, v109
	v_fmac_f32_e32 v2, v81, v110
	v_fmac_f32_e32 v3, v81, v111
	v_fmac_f32_e32 v4, v81, v112
	v_fmac_f32_e32 v5, v81, v113
	v_fmac_f32_e32 v6, v81, v114
	v_fmac_f32_e32 v7, v81, v115
	v_fmac_f32_e32 v8, v81, v116
	ds_read_b128 v[96:99], v9 offset:3328
	ds_read_b128 v[100:103], v9 offset:3344
	ds_read_b32 v104, v9 offset:3360
	ds_read_b128 v[108:111], v9 offset:3392
	ds_read_b128 v[112:115], v9 offset:3408
	ds_read_b32 v116, v9 offset:3424
	s_waitcnt lgkmcnt(6)
	v_fmac_f32_e32 v0, v82, v120
	v_fmac_f32_e32 v1, v82, v121
	v_fmac_f32_e32 v2, v82, v122
	v_fmac_f32_e32 v3, v82, v123
	v_fmac_f32_e32 v4, v82, v124
	v_fmac_f32_e32 v5, v82, v125
	v_fmac_f32_e32 v6, v82, v126
	v_fmac_f32_e32 v7, v82, v127
	v_fmac_f32_e32 v8, v82, v128
	v_fmac_f32_e32 v0, v83, v132
	v_fmac_f32_e32 v1, v83, v133
	v_fmac_f32_e32 v2, v83, v134
	v_fmac_f32_e32 v3, v83, v135
	v_fmac_f32_e32 v4, v83, v136
	v_fmac_f32_e32 v5, v83, v137
	v_fmac_f32_e32 v6, v83, v138
	v_fmac_f32_e32 v7, v83, v139
	v_fmac_f32_e32 v8, v83, v140
	ds_read_b128 v[120:123], v9 offset:3456
	ds_read_b128 v[124:127], v9 offset:3472
	ds_read_b32 v128, v9 offset:3488
	ds_read_b128 v[132:135], v9 offset:3520
	ds_read_b128 v[136:139], v9 offset:3536
	ds_read_b32 v140, v9 offset:3552
	s_waitcnt lgkmcnt(6)
	v_fmac_f32_e32 v0, v84, v96
	v_fmac_f32_e32 v1, v84, v97
	v_fmac_f32_e32 v2, v84, v98
	v_fmac_f32_e32 v3, v84, v99
	v_fmac_f32_e32 v4, v84, v100
	v_fmac_f32_e32 v5, v84, v101
	v_fmac_f32_e32 v6, v84, v102
	v_fmac_f32_e32 v7, v84, v103
	v_fmac_f32_e32 v8, v84, v104
	v_fmac_f32_e32 v0, v85, v108
	v_fmac_f32_e32 v1, v85, v109
	v_fmac_f32_e32 v2, v85, v110
	v_fmac_f32_e32 v3, v85, v111
	v_fmac_f32_e32 v4, v85, v112
	v_fmac_f32_e32 v5, v85, v113
	v_fmac_f32_e32 v6, v85, v114
	v_fmac_f32_e32 v7, v85, v115
	v_fmac_f32_e32 v8, v85, v116
	ds_read_b128 v[96:99], v9 offset:3584
	ds_read_b128 v[100:103], v9 offset:3600
	ds_read_b32 v104, v9 offset:3616
	ds_read_b128 v[108:111], v9 offset:3648
	ds_read_b128 v[112:115], v9 offset:3664
	ds_read_b32 v116, v9 offset:3680
	s_waitcnt lgkmcnt(6)
	v_fmac_f32_e32 v0, v86, v120
	v_fmac_f32_e32 v1, v86, v121
	v_fmac_f32_e32 v2, v86, v122
	v_fmac_f32_e32 v3, v86, v123
	v_fmac_f32_e32 v4, v86, v124
	v_fmac_f32_e32 v5, v86, v125
	v_fmac_f32_e32 v6, v86, v126
	v_fmac_f32_e32 v7, v86, v127
	v_fmac_f32_e32 v8, v86, v128
	v_fmac_f32_e32 v0, v87, v132
	v_fmac_f32_e32 v1, v87, v133
	v_fmac_f32_e32 v2, v87, v134
	v_fmac_f32_e32 v3, v87, v135
	v_fmac_f32_e32 v4, v87, v136
	v_fmac_f32_e32 v5, v87, v137
	v_fmac_f32_e32 v6, v87, v138
	v_fmac_f32_e32 v7, v87, v139
	v_fmac_f32_e32 v8, v87, v140
	ds_read_b128 v[120:123], v9 offset:3712
	ds_read_b128 v[124:127], v9 offset:3728
	ds_read_b32 v128, v9 offset:3744
	ds_read_b128 v[132:135], v9 offset:3776
	ds_read_b128 v[136:139], v9 offset:3792
	ds_read_b32 v140, v9 offset:3808
	s_waitcnt lgkmcnt(6)
	v_fmac_f32_e32 v0, v88, v96
	v_fmac_f32_e32 v1, v88, v97
	v_fmac_f32_e32 v2, v88, v98
	v_fmac_f32_e32 v3, v88, v99
	v_fmac_f32_e32 v4, v88, v100
	v_fmac_f32_e32 v5, v88, v101
	v_fmac_f32_e32 v6, v88, v102
	v_fmac_f32_e32 v7, v88, v103
	v_fmac_f32_e32 v8, v88, v104
	v_fmac_f32_e32 v0, v89, v108
	v_fmac_f32_e32 v1, v89, v109
	v_fmac_f32_e32 v2, v89, v110
	v_fmac_f32_e32 v3, v89, v111
	v_fmac_f32_e32 v4, v89, v112
	v_fmac_f32_e32 v5, v89, v113
	v_fmac_f32_e32 v6, v89, v114
	v_fmac_f32_e32 v7, v89, v115
	v_fmac_f32_e32 v8, v89, v116
	ds_read_b128 v[96:99], v9 offset:3840
	ds_read_b128 v[100:103], v9 offset:3856
	ds_read_b32 v104, v9 offset:3872
	ds_read_b128 v[108:111], v9 offset:3904
	ds_read_b128 v[112:115], v9 offset:3920
	ds_read_b32 v116, v9 offset:3936
	s_waitcnt lgkmcnt(6)
	v_fmac_f32_e32 v0, v90, v120
	v_fmac_f32_e32 v1, v90, v121
	v_fmac_f32_e32 v2, v90, v122
	v_fmac_f32_e32 v3, v90, v123
	v_fmac_f32_e32 v4, v90, v124
	v_fmac_f32_e32 v5, v90, v125
	v_fmac_f32_e32 v6, v90, v126
	v_fmac_f32_e32 v7, v90, v127
	v_fmac_f32_e32 v8, v90, v128
	v_fmac_f32_e32 v0, v91, v132
	v_fmac_f32_e32 v1, v91, v133
	v_fmac_f32_e32 v2, v91, v134
	v_fmac_f32_e32 v3, v91, v135
	v_fmac_f32_e32 v4, v91, v136
	v_fmac_f32_e32 v5, v91, v137
	v_fmac_f32_e32 v6, v91, v138
	v_fmac_f32_e32 v7, v91, v139
	v_fmac_f32_e32 v8, v91, v140
	ds_read_b128 v[120:123], v9 offset:3968
	ds_read_b128 v[124:127], v9 offset:3984
	ds_read_b32 v128, v9 offset:4000
	ds_read_b128 v[132:135], v9 offset:4032
	ds_read_b128 v[136:139], v9 offset:4048
	ds_read_b32 v140, v9 offset:4064
	s_waitcnt lgkmcnt(6)
	v_fmac_f32_e32 v0, v92, v96
	v_fmac_f32_e32 v1, v92, v97
	v_fmac_f32_e32 v2, v92, v98
	v_fmac_f32_e32 v3, v92, v99
	v_fmac_f32_e32 v4, v92, v100
	v_fmac_f32_e32 v5, v92, v101
	v_fmac_f32_e32 v6, v92, v102
	v_fmac_f32_e32 v7, v92, v103
	v_fmac_f32_e32 v8, v92, v104
	v_fmac_f32_e32 v0, v93, v108
	v_fmac_f32_e32 v1, v93, v109
	v_fmac_f32_e32 v2, v93, v110
	v_fmac_f32_e32 v3, v93, v111
	v_fmac_f32_e32 v4, v93, v112
	v_fmac_f32_e32 v5, v93, v113
	v_fmac_f32_e32 v6, v93, v114
	v_fmac_f32_e32 v7, v93, v115
	v_fmac_f32_e32 v8, v93, v116
	ds_read_b128 v[96:99], v9 offset:4096
	ds_read_b128 v[100:103], v9 offset:4112
	ds_read_b32 v104, v9 offset:4128
	ds_read_b128 v[108:111], v9 offset:4160
	ds_read_b128 v[112:115], v9 offset:4176
	ds_read_b32 v116, v9 offset:4192
	s_waitcnt lgkmcnt(6)
	v_fmac_f32_e32 v0, v94, v120
	v_fmac_f32_e32 v1, v94, v121
	v_fmac_f32_e32 v2, v94, v122
	v_fmac_f32_e32 v3, v94, v123
	v_fmac_f32_e32 v4, v94, v124
	v_fmac_f32_e32 v5, v94, v125
	v_fmac_f32_e32 v6, v94, v126
	v_fmac_f32_e32 v7, v94, v127
	v_fmac_f32_e32 v8, v94, v128
	v_fmac_f32_e32 v0, v95, v132
	v_fmac_f32_e32 v1, v95, v133
	v_fmac_f32_e32 v2, v95, v134
	v_fmac_f32_e32 v3, v95, v135
	v_fmac_f32_e32 v4, v95, v136
	v_fmac_f32_e32 v5, v95, v137
	v_fmac_f32_e32 v6, v95, v138
	v_fmac_f32_e32 v7, v95, v139
	v_fmac_f32_e32 v8, v95, v140
	s_waitcnt vmcnt(32)
	global_load_dword v80, v30, s[28:29]
	s_add_u32 s28, s28, 0x6000
	s_addc_u32 s29, s29, 0
	global_load_dword v81, v30, s[28:29]
	s_add_u32 s28, s28, 0x6000
	s_addc_u32 s29, s29, 0
	global_load_dword v82, v30, s[28:29]
	s_add_u32 s28, s28, 0x6000
	s_addc_u32 s29, s29, 0
	global_load_dword v83, v30, s[28:29]
	s_add_u32 s28, s28, 0x6000
	s_addc_u32 s29, s29, 0
	global_load_dword v84, v30, s[28:29]
	s_add_u32 s28, s28, 0x6000
	s_addc_u32 s29, s29, 0
	global_load_dword v85, v30, s[28:29]
	s_add_u32 s28, s28, 0x6000
	s_addc_u32 s29, s29, 0
	global_load_dword v86, v30, s[28:29]
	s_add_u32 s28, s28, 0x6000
	s_addc_u32 s29, s29, 0
	global_load_dword v87, v30, s[28:29]
	s_add_u32 s28, s28, 0x6000
	s_addc_u32 s29, s29, 0
	global_load_dword v88, v30, s[28:29]
	s_add_u32 s28, s28, 0x6000
	s_addc_u32 s29, s29, 0
	global_load_dword v89, v30, s[28:29]
	s_add_u32 s28, s28, 0x6000
	s_addc_u32 s29, s29, 0
	global_load_dword v90, v30, s[28:29]
	s_add_u32 s28, s28, 0x6000
	s_addc_u32 s29, s29, 0
	global_load_dword v91, v30, s[28:29]
	s_add_u32 s28, s28, 0x6000
	s_addc_u32 s29, s29, 0
	global_load_dword v92, v30, s[28:29]
	s_add_u32 s28, s28, 0x6000
	s_addc_u32 s29, s29, 0
	global_load_dword v93, v30, s[28:29]
	s_add_u32 s28, s28, 0x6000
	s_addc_u32 s29, s29, 0
	global_load_dword v94, v30, s[28:29]
	s_add_u32 s28, s28, 0x6000
	s_addc_u32 s29, s29, 0
	global_load_dword v95, v30, s[28:29]
	s_add_u32 s28, s28, 0x6000
	s_addc_u32 s29, s29, 0
	ds_read_b128 v[120:123], v9 offset:4224
	ds_read_b128 v[124:127], v9 offset:4240
	ds_read_b32 v128, v9 offset:4256
	ds_read_b128 v[132:135], v9 offset:4288
	ds_read_b128 v[136:139], v9 offset:4304
	ds_read_b32 v140, v9 offset:4320
	s_waitcnt lgkmcnt(6)
	v_fmac_f32_e32 v0, v32, v96
	v_fmac_f32_e32 v1, v32, v97
	v_fmac_f32_e32 v2, v32, v98
	v_fmac_f32_e32 v3, v32, v99
	v_fmac_f32_e32 v4, v32, v100
	v_fmac_f32_e32 v5, v32, v101
	v_fmac_f32_e32 v6, v32, v102
	v_fmac_f32_e32 v7, v32, v103
	v_fmac_f32_e32 v8, v32, v104
	v_fmac_f32_e32 v0, v33, v108
	v_fmac_f32_e32 v1, v33, v109
	v_fmac_f32_e32 v2, v33, v110
	v_fmac_f32_e32 v3, v33, v111
	v_fmac_f32_e32 v4, v33, v112
	v_fmac_f32_e32 v5, v33, v113
	v_fmac_f32_e32 v6, v33, v114
	v_fmac_f32_e32 v7, v33, v115
	v_fmac_f32_e32 v8, v33, v116
	ds_read_b128 v[96:99], v9 offset:4352
	ds_read_b128 v[100:103], v9 offset:4368
	ds_read_b32 v104, v9 offset:4384
	ds_read_b128 v[108:111], v9 offset:4416
	ds_read_b128 v[112:115], v9 offset:4432
	ds_read_b32 v116, v9 offset:4448
	s_waitcnt lgkmcnt(6)
	v_fmac_f32_e32 v0, v34, v120
	v_fmac_f32_e32 v1, v34, v121
	v_fmac_f32_e32 v2, v34, v122
	v_fmac_f32_e32 v3, v34, v123
	v_fmac_f32_e32 v4, v34, v124
	v_fmac_f32_e32 v5, v34, v125
	v_fmac_f32_e32 v6, v34, v126
	v_fmac_f32_e32 v7, v34, v127
	v_fmac_f32_e32 v8, v34, v128
	v_fmac_f32_e32 v0, v35, v132
	v_fmac_f32_e32 v1, v35, v133
	v_fmac_f32_e32 v2, v35, v134
	v_fmac_f32_e32 v3, v35, v135
	v_fmac_f32_e32 v4, v35, v136
	v_fmac_f32_e32 v5, v35, v137
	v_fmac_f32_e32 v6, v35, v138
	v_fmac_f32_e32 v7, v35, v139
	v_fmac_f32_e32 v8, v35, v140
	ds_read_b128 v[120:123], v9 offset:4480
	ds_read_b128 v[124:127], v9 offset:4496
	ds_read_b32 v128, v9 offset:4512
	ds_read_b128 v[132:135], v9 offset:4544
	ds_read_b128 v[136:139], v9 offset:4560
	ds_read_b32 v140, v9 offset:4576
	s_waitcnt lgkmcnt(6)
	v_fmac_f32_e32 v0, v36, v96
	v_fmac_f32_e32 v1, v36, v97
	v_fmac_f32_e32 v2, v36, v98
	v_fmac_f32_e32 v3, v36, v99
	v_fmac_f32_e32 v4, v36, v100
	v_fmac_f32_e32 v5, v36, v101
	v_fmac_f32_e32 v6, v36, v102
	v_fmac_f32_e32 v7, v36, v103
	v_fmac_f32_e32 v8, v36, v104
	v_fmac_f32_e32 v0, v37, v108
	v_fmac_f32_e32 v1, v37, v109
	v_fmac_f32_e32 v2, v37, v110
	v_fmac_f32_e32 v3, v37, v111
	v_fmac_f32_e32 v4, v37, v112
	v_fmac_f32_e32 v5, v37, v113
	v_fmac_f32_e32 v6, v37, v114
	v_fmac_f32_e32 v7, v37, v115
	v_fmac_f32_e32 v8, v37, v116
	ds_read_b128 v[96:99], v9 offset:4608
	ds_read_b128 v[100:103], v9 offset:4624
	ds_read_b32 v104, v9 offset:4640
	ds_read_b128 v[108:111], v9 offset:4672
	ds_read_b128 v[112:115], v9 offset:4688
	ds_read_b32 v116, v9 offset:4704
	s_waitcnt lgkmcnt(6)
	v_fmac_f32_e32 v0, v38, v120
	v_fmac_f32_e32 v1, v38, v121
	v_fmac_f32_e32 v2, v38, v122
	v_fmac_f32_e32 v3, v38, v123
	v_fmac_f32_e32 v4, v38, v124
	v_fmac_f32_e32 v5, v38, v125
	v_fmac_f32_e32 v6, v38, v126
	v_fmac_f32_e32 v7, v38, v127
	v_fmac_f32_e32 v8, v38, v128
	v_fmac_f32_e32 v0, v39, v132
	v_fmac_f32_e32 v1, v39, v133
	v_fmac_f32_e32 v2, v39, v134
	v_fmac_f32_e32 v3, v39, v135
	v_fmac_f32_e32 v4, v39, v136
	v_fmac_f32_e32 v5, v39, v137
	v_fmac_f32_e32 v6, v39, v138
	v_fmac_f32_e32 v7, v39, v139
	v_fmac_f32_e32 v8, v39, v140
	ds_read_b128 v[120:123], v9 offset:4736
	ds_read_b128 v[124:127], v9 offset:4752
	ds_read_b32 v128, v9 offset:4768
	ds_read_b128 v[132:135], v9 offset:4800
	ds_read_b128 v[136:139], v9 offset:4816
	ds_read_b32 v140, v9 offset:4832
	s_waitcnt lgkmcnt(6)
	v_fmac_f32_e32 v0, v40, v96
	v_fmac_f32_e32 v1, v40, v97
	v_fmac_f32_e32 v2, v40, v98
	v_fmac_f32_e32 v3, v40, v99
	v_fmac_f32_e32 v4, v40, v100
	v_fmac_f32_e32 v5, v40, v101
	v_fmac_f32_e32 v6, v40, v102
	v_fmac_f32_e32 v7, v40, v103
	v_fmac_f32_e32 v8, v40, v104
	v_fmac_f32_e32 v0, v41, v108
	v_fmac_f32_e32 v1, v41, v109
	v_fmac_f32_e32 v2, v41, v110
	v_fmac_f32_e32 v3, v41, v111
	v_fmac_f32_e32 v4, v41, v112
	v_fmac_f32_e32 v5, v41, v113
	v_fmac_f32_e32 v6, v41, v114
	v_fmac_f32_e32 v7, v41, v115
	v_fmac_f32_e32 v8, v41, v116
	ds_read_b128 v[96:99], v9 offset:4864
	ds_read_b128 v[100:103], v9 offset:4880
	ds_read_b32 v104, v9 offset:4896
	ds_read_b128 v[108:111], v9 offset:4928
	ds_read_b128 v[112:115], v9 offset:4944
	ds_read_b32 v116, v9 offset:4960
	s_waitcnt lgkmcnt(6)
	v_fmac_f32_e32 v0, v42, v120
	v_fmac_f32_e32 v1, v42, v121
	v_fmac_f32_e32 v2, v42, v122
	v_fmac_f32_e32 v3, v42, v123
	v_fmac_f32_e32 v4, v42, v124
	v_fmac_f32_e32 v5, v42, v125
	v_fmac_f32_e32 v6, v42, v126
	v_fmac_f32_e32 v7, v42, v127
	v_fmac_f32_e32 v8, v42, v128
	v_fmac_f32_e32 v0, v43, v132
	v_fmac_f32_e32 v1, v43, v133
	v_fmac_f32_e32 v2, v43, v134
	v_fmac_f32_e32 v3, v43, v135
	v_fmac_f32_e32 v4, v43, v136
	v_fmac_f32_e32 v5, v43, v137
	v_fmac_f32_e32 v6, v43, v138
	v_fmac_f32_e32 v7, v43, v139
	v_fmac_f32_e32 v8, v43, v140
	ds_read_b128 v[120:123], v9 offset:4992
	ds_read_b128 v[124:127], v9 offset:5008
	ds_read_b32 v128, v9 offset:5024
	ds_read_b128 v[132:135], v9 offset:5056
	ds_read_b128 v[136:139], v9 offset:5072
	ds_read_b32 v140, v9 offset:5088
	s_waitcnt lgkmcnt(6)
	v_fmac_f32_e32 v0, v44, v96
	v_fmac_f32_e32 v1, v44, v97
	v_fmac_f32_e32 v2, v44, v98
	v_fmac_f32_e32 v3, v44, v99
	v_fmac_f32_e32 v4, v44, v100
	v_fmac_f32_e32 v5, v44, v101
	v_fmac_f32_e32 v6, v44, v102
	v_fmac_f32_e32 v7, v44, v103
	v_fmac_f32_e32 v8, v44, v104
	v_fmac_f32_e32 v0, v45, v108
	v_fmac_f32_e32 v1, v45, v109
	v_fmac_f32_e32 v2, v45, v110
	v_fmac_f32_e32 v3, v45, v111
	v_fmac_f32_e32 v4, v45, v112
	v_fmac_f32_e32 v5, v45, v113
	v_fmac_f32_e32 v6, v45, v114
	v_fmac_f32_e32 v7, v45, v115
	v_fmac_f32_e32 v8, v45, v116
	ds_read_b128 v[96:99], v9 offset:5120
	ds_read_b128 v[100:103], v9 offset:5136
	ds_read_b32 v104, v9 offset:5152
	ds_read_b128 v[108:111], v9 offset:5184
	ds_read_b128 v[112:115], v9 offset:5200
	ds_read_b32 v116, v9 offset:5216
	s_waitcnt lgkmcnt(6)
	v_fmac_f32_e32 v0, v46, v120
	v_fmac_f32_e32 v1, v46, v121
	v_fmac_f32_e32 v2, v46, v122
	v_fmac_f32_e32 v3, v46, v123
	v_fmac_f32_e32 v4, v46, v124
	v_fmac_f32_e32 v5, v46, v125
	v_fmac_f32_e32 v6, v46, v126
	v_fmac_f32_e32 v7, v46, v127
	v_fmac_f32_e32 v8, v46, v128
	v_fmac_f32_e32 v0, v47, v132
	v_fmac_f32_e32 v1, v47, v133
	v_fmac_f32_e32 v2, v47, v134
	v_fmac_f32_e32 v3, v47, v135
	v_fmac_f32_e32 v4, v47, v136
	v_fmac_f32_e32 v5, v47, v137
	v_fmac_f32_e32 v6, v47, v138
	v_fmac_f32_e32 v7, v47, v139
	v_fmac_f32_e32 v8, v47, v140
	s_waitcnt vmcnt(32)
	ds_read_b128 v[120:123], v9 offset:5248
	ds_read_b128 v[124:127], v9 offset:5264
	ds_read_b32 v128, v9 offset:5280
	ds_read_b128 v[132:135], v9 offset:5312
	ds_read_b128 v[136:139], v9 offset:5328
	ds_read_b32 v140, v9 offset:5344
	s_waitcnt lgkmcnt(6)
	v_fmac_f32_e32 v0, v48, v96
	v_fmac_f32_e32 v1, v48, v97
	v_fmac_f32_e32 v2, v48, v98
	v_fmac_f32_e32 v3, v48, v99
	v_fmac_f32_e32 v4, v48, v100
	v_fmac_f32_e32 v5, v48, v101
	v_fmac_f32_e32 v6, v48, v102
	v_fmac_f32_e32 v7, v48, v103
	v_fmac_f32_e32 v8, v48, v104
	v_fmac_f32_e32 v0, v49, v108
	v_fmac_f32_e32 v1, v49, v109
	v_fmac_f32_e32 v2, v49, v110
	v_fmac_f32_e32 v3, v49, v111
	v_fmac_f32_e32 v4, v49, v112
	v_fmac_f32_e32 v5, v49, v113
	v_fmac_f32_e32 v6, v49, v114
	v_fmac_f32_e32 v7, v49, v115
	v_fmac_f32_e32 v8, v49, v116
	ds_read_b128 v[96:99], v9 offset:5376
	ds_read_b128 v[100:103], v9 offset:5392
	ds_read_b32 v104, v9 offset:5408
	ds_read_b128 v[108:111], v9 offset:5440
	ds_read_b128 v[112:115], v9 offset:5456
	ds_read_b32 v116, v9 offset:5472
	s_waitcnt lgkmcnt(6)
	v_fmac_f32_e32 v0, v50, v120
	v_fmac_f32_e32 v1, v50, v121
	v_fmac_f32_e32 v2, v50, v122
	v_fmac_f32_e32 v3, v50, v123
	v_fmac_f32_e32 v4, v50, v124
	v_fmac_f32_e32 v5, v50, v125
	v_fmac_f32_e32 v6, v50, v126
	v_fmac_f32_e32 v7, v50, v127
	v_fmac_f32_e32 v8, v50, v128
	v_fmac_f32_e32 v0, v51, v132
	v_fmac_f32_e32 v1, v51, v133
	v_fmac_f32_e32 v2, v51, v134
	v_fmac_f32_e32 v3, v51, v135
	v_fmac_f32_e32 v4, v51, v136
	v_fmac_f32_e32 v5, v51, v137
	v_fmac_f32_e32 v6, v51, v138
	v_fmac_f32_e32 v7, v51, v139
	v_fmac_f32_e32 v8, v51, v140
	ds_read_b128 v[120:123], v9 offset:5504
	ds_read_b128 v[124:127], v9 offset:5520
	ds_read_b32 v128, v9 offset:5536
	ds_read_b128 v[132:135], v9 offset:5568
	ds_read_b128 v[136:139], v9 offset:5584
	ds_read_b32 v140, v9 offset:5600
	s_waitcnt lgkmcnt(6)
	v_fmac_f32_e32 v0, v52, v96
	v_fmac_f32_e32 v1, v52, v97
	v_fmac_f32_e32 v2, v52, v98
	v_fmac_f32_e32 v3, v52, v99
	v_fmac_f32_e32 v4, v52, v100
	v_fmac_f32_e32 v5, v52, v101
	v_fmac_f32_e32 v6, v52, v102
	v_fmac_f32_e32 v7, v52, v103
	v_fmac_f32_e32 v8, v52, v104
	v_fmac_f32_e32 v0, v53, v108
	v_fmac_f32_e32 v1, v53, v109
	v_fmac_f32_e32 v2, v53, v110
	v_fmac_f32_e32 v3, v53, v111
	v_fmac_f32_e32 v4, v53, v112
	v_fmac_f32_e32 v5, v53, v113
	v_fmac_f32_e32 v6, v53, v114
	v_fmac_f32_e32 v7, v53, v115
	v_fmac_f32_e32 v8, v53, v116
	ds_read_b128 v[96:99], v9 offset:5632
	ds_read_b128 v[100:103], v9 offset:5648
	ds_read_b32 v104, v9 offset:5664
	ds_read_b128 v[108:111], v9 offset:5696
	ds_read_b128 v[112:115], v9 offset:5712
	ds_read_b32 v116, v9 offset:5728
	s_waitcnt lgkmcnt(6)
	v_fmac_f32_e32 v0, v54, v120
	v_fmac_f32_e32 v1, v54, v121
	v_fmac_f32_e32 v2, v54, v122
	v_fmac_f32_e32 v3, v54, v123
	v_fmac_f32_e32 v4, v54, v124
	v_fmac_f32_e32 v5, v54, v125
	v_fmac_f32_e32 v6, v54, v126
	v_fmac_f32_e32 v7, v54, v127
	v_fmac_f32_e32 v8, v54, v128
	v_fmac_f32_e32 v0, v55, v132
	v_fmac_f32_e32 v1, v55, v133
	v_fmac_f32_e32 v2, v55, v134
	v_fmac_f32_e32 v3, v55, v135
	v_fmac_f32_e32 v4, v55, v136
	v_fmac_f32_e32 v5, v55, v137
	v_fmac_f32_e32 v6, v55, v138
	v_fmac_f32_e32 v7, v55, v139
	v_fmac_f32_e32 v8, v55, v140
	ds_read_b128 v[120:123], v9 offset:5760
	ds_read_b128 v[124:127], v9 offset:5776
	ds_read_b32 v128, v9 offset:5792
	ds_read_b128 v[132:135], v9 offset:5824
	ds_read_b128 v[136:139], v9 offset:5840
	ds_read_b32 v140, v9 offset:5856
	s_waitcnt lgkmcnt(6)
	v_fmac_f32_e32 v0, v56, v96
	v_fmac_f32_e32 v1, v56, v97
	v_fmac_f32_e32 v2, v56, v98
	v_fmac_f32_e32 v3, v56, v99
	v_fmac_f32_e32 v4, v56, v100
	v_fmac_f32_e32 v5, v56, v101
	v_fmac_f32_e32 v6, v56, v102
	v_fmac_f32_e32 v7, v56, v103
	v_fmac_f32_e32 v8, v56, v104
	v_fmac_f32_e32 v0, v57, v108
	v_fmac_f32_e32 v1, v57, v109
	v_fmac_f32_e32 v2, v57, v110
	v_fmac_f32_e32 v3, v57, v111
	v_fmac_f32_e32 v4, v57, v112
	v_fmac_f32_e32 v5, v57, v113
	v_fmac_f32_e32 v6, v57, v114
	v_fmac_f32_e32 v7, v57, v115
	v_fmac_f32_e32 v8, v57, v116
	ds_read_b128 v[96:99], v9 offset:5888
	ds_read_b128 v[100:103], v9 offset:5904
	ds_read_b32 v104, v9 offset:5920
	ds_read_b128 v[108:111], v9 offset:5952
	ds_read_b128 v[112:115], v9 offset:5968
	ds_read_b32 v116, v9 offset:5984
	s_waitcnt lgkmcnt(6)
	v_fmac_f32_e32 v0, v58, v120
	v_fmac_f32_e32 v1, v58, v121
	v_fmac_f32_e32 v2, v58, v122
	v_fmac_f32_e32 v3, v58, v123
	v_fmac_f32_e32 v4, v58, v124
	v_fmac_f32_e32 v5, v58, v125
	v_fmac_f32_e32 v6, v58, v126
	v_fmac_f32_e32 v7, v58, v127
	v_fmac_f32_e32 v8, v58, v128
	v_fmac_f32_e32 v0, v59, v132
	v_fmac_f32_e32 v1, v59, v133
	v_fmac_f32_e32 v2, v59, v134
	v_fmac_f32_e32 v3, v59, v135
	v_fmac_f32_e32 v4, v59, v136
	v_fmac_f32_e32 v5, v59, v137
	v_fmac_f32_e32 v6, v59, v138
	v_fmac_f32_e32 v7, v59, v139
	v_fmac_f32_e32 v8, v59, v140
	ds_read_b128 v[120:123], v9 offset:6016
	ds_read_b128 v[124:127], v9 offset:6032
	ds_read_b32 v128, v9 offset:6048
	ds_read_b128 v[132:135], v9 offset:6080
	ds_read_b128 v[136:139], v9 offset:6096
	ds_read_b32 v140, v9 offset:6112
	s_waitcnt lgkmcnt(6)
	v_fmac_f32_e32 v0, v60, v96
	v_fmac_f32_e32 v1, v60, v97
	v_fmac_f32_e32 v2, v60, v98
	v_fmac_f32_e32 v3, v60, v99
	v_fmac_f32_e32 v4, v60, v100
	v_fmac_f32_e32 v5, v60, v101
	v_fmac_f32_e32 v6, v60, v102
	v_fmac_f32_e32 v7, v60, v103
	v_fmac_f32_e32 v8, v60, v104
	v_fmac_f32_e32 v0, v61, v108
	v_fmac_f32_e32 v1, v61, v109
	v_fmac_f32_e32 v2, v61, v110
	v_fmac_f32_e32 v3, v61, v111
	v_fmac_f32_e32 v4, v61, v112
	v_fmac_f32_e32 v5, v61, v113
	v_fmac_f32_e32 v6, v61, v114
	v_fmac_f32_e32 v7, v61, v115
	v_fmac_f32_e32 v8, v61, v116
	ds_read_b128 v[96:99], v9 offset:6144
	ds_read_b128 v[100:103], v9 offset:6160
	ds_read_b32 v104, v9 offset:6176
	ds_read_b128 v[108:111], v9 offset:6208
	ds_read_b128 v[112:115], v9 offset:6224
	ds_read_b32 v116, v9 offset:6240
	s_waitcnt lgkmcnt(6)
	v_fmac_f32_e32 v0, v62, v120
	v_fmac_f32_e32 v1, v62, v121
	v_fmac_f32_e32 v2, v62, v122
	v_fmac_f32_e32 v3, v62, v123
	v_fmac_f32_e32 v4, v62, v124
	v_fmac_f32_e32 v5, v62, v125
	v_fmac_f32_e32 v6, v62, v126
	v_fmac_f32_e32 v7, v62, v127
	v_fmac_f32_e32 v8, v62, v128
	v_fmac_f32_e32 v0, v63, v132
	v_fmac_f32_e32 v1, v63, v133
	v_fmac_f32_e32 v2, v63, v134
	v_fmac_f32_e32 v3, v63, v135
	v_fmac_f32_e32 v4, v63, v136
	v_fmac_f32_e32 v5, v63, v137
	v_fmac_f32_e32 v6, v63, v138
	v_fmac_f32_e32 v7, v63, v139
	v_fmac_f32_e32 v8, v63, v140
	s_waitcnt vmcnt(16)
	ds_read_b128 v[120:123], v9 offset:6272
	ds_read_b128 v[124:127], v9 offset:6288
	ds_read_b32 v128, v9 offset:6304
	ds_read_b128 v[132:135], v9 offset:6336
	ds_read_b128 v[136:139], v9 offset:6352
	ds_read_b32 v140, v9 offset:6368
	s_waitcnt lgkmcnt(6)
	v_fmac_f32_e32 v0, v64, v96
	v_fmac_f32_e32 v1, v64, v97
	v_fmac_f32_e32 v2, v64, v98
	v_fmac_f32_e32 v3, v64, v99
	v_fmac_f32_e32 v4, v64, v100
	v_fmac_f32_e32 v5, v64, v101
	v_fmac_f32_e32 v6, v64, v102
	v_fmac_f32_e32 v7, v64, v103
	v_fmac_f32_e32 v8, v64, v104
	v_fmac_f32_e32 v0, v65, v108
	v_fmac_f32_e32 v1, v65, v109
	v_fmac_f32_e32 v2, v65, v110
	v_fmac_f32_e32 v3, v65, v111
	v_fmac_f32_e32 v4, v65, v112
	v_fmac_f32_e32 v5, v65, v113
	v_fmac_f32_e32 v6, v65, v114
	v_fmac_f32_e32 v7, v65, v115
	v_fmac_f32_e32 v8, v65, v116
	ds_read_b128 v[96:99], v9 offset:6400
	ds_read_b128 v[100:103], v9 offset:6416
	ds_read_b32 v104, v9 offset:6432
	ds_read_b128 v[108:111], v9 offset:6464
	ds_read_b128 v[112:115], v9 offset:6480
	ds_read_b32 v116, v9 offset:6496
	s_waitcnt lgkmcnt(6)
	v_fmac_f32_e32 v0, v66, v120
	v_fmac_f32_e32 v1, v66, v121
	v_fmac_f32_e32 v2, v66, v122
	v_fmac_f32_e32 v3, v66, v123
	v_fmac_f32_e32 v4, v66, v124
	v_fmac_f32_e32 v5, v66, v125
	v_fmac_f32_e32 v6, v66, v126
	v_fmac_f32_e32 v7, v66, v127
	v_fmac_f32_e32 v8, v66, v128
	v_fmac_f32_e32 v0, v67, v132
	v_fmac_f32_e32 v1, v67, v133
	v_fmac_f32_e32 v2, v67, v134
	v_fmac_f32_e32 v3, v67, v135
	v_fmac_f32_e32 v4, v67, v136
	v_fmac_f32_e32 v5, v67, v137
	v_fmac_f32_e32 v6, v67, v138
	v_fmac_f32_e32 v7, v67, v139
	v_fmac_f32_e32 v8, v67, v140
	ds_read_b128 v[120:123], v9 offset:6528
	ds_read_b128 v[124:127], v9 offset:6544
	ds_read_b32 v128, v9 offset:6560
	ds_read_b128 v[132:135], v9 offset:6592
	ds_read_b128 v[136:139], v9 offset:6608
	ds_read_b32 v140, v9 offset:6624
	s_waitcnt lgkmcnt(6)
	v_fmac_f32_e32 v0, v68, v96
	v_fmac_f32_e32 v1, v68, v97
	v_fmac_f32_e32 v2, v68, v98
	v_fmac_f32_e32 v3, v68, v99
	v_fmac_f32_e32 v4, v68, v100
	v_fmac_f32_e32 v5, v68, v101
	v_fmac_f32_e32 v6, v68, v102
	v_fmac_f32_e32 v7, v68, v103
	v_fmac_f32_e32 v8, v68, v104
	v_fmac_f32_e32 v0, v69, v108
	v_fmac_f32_e32 v1, v69, v109
	v_fmac_f32_e32 v2, v69, v110
	v_fmac_f32_e32 v3, v69, v111
	v_fmac_f32_e32 v4, v69, v112
	v_fmac_f32_e32 v5, v69, v113
	v_fmac_f32_e32 v6, v69, v114
	v_fmac_f32_e32 v7, v69, v115
	v_fmac_f32_e32 v8, v69, v116
	ds_read_b128 v[96:99], v9 offset:6656
	ds_read_b128 v[100:103], v9 offset:6672
	ds_read_b32 v104, v9 offset:6688
	ds_read_b128 v[108:111], v9 offset:6720
	ds_read_b128 v[112:115], v9 offset:6736
	ds_read_b32 v116, v9 offset:6752
	s_waitcnt lgkmcnt(6)
	v_fmac_f32_e32 v0, v70, v120
	v_fmac_f32_e32 v1, v70, v121
	v_fmac_f32_e32 v2, v70, v122
	v_fmac_f32_e32 v3, v70, v123
	v_fmac_f32_e32 v4, v70, v124
	v_fmac_f32_e32 v5, v70, v125
	v_fmac_f32_e32 v6, v70, v126
	v_fmac_f32_e32 v7, v70, v127
	v_fmac_f32_e32 v8, v70, v128
	v_fmac_f32_e32 v0, v71, v132
	v_fmac_f32_e32 v1, v71, v133
	v_fmac_f32_e32 v2, v71, v134
	v_fmac_f32_e32 v3, v71, v135
	v_fmac_f32_e32 v4, v71, v136
	v_fmac_f32_e32 v5, v71, v137
	v_fmac_f32_e32 v6, v71, v138
	v_fmac_f32_e32 v7, v71, v139
	v_fmac_f32_e32 v8, v71, v140
	ds_read_b128 v[120:123], v9 offset:6784
	ds_read_b128 v[124:127], v9 offset:6800
	ds_read_b32 v128, v9 offset:6816
	ds_read_b128 v[132:135], v9 offset:6848
	ds_read_b128 v[136:139], v9 offset:6864
	ds_read_b32 v140, v9 offset:6880
	s_waitcnt lgkmcnt(6)
	v_fmac_f32_e32 v0, v72, v96
	v_fmac_f32_e32 v1, v72, v97
	v_fmac_f32_e32 v2, v72, v98
	v_fmac_f32_e32 v3, v72, v99
	v_fmac_f32_e32 v4, v72, v100
	v_fmac_f32_e32 v5, v72, v101
	v_fmac_f32_e32 v6, v72, v102
	v_fmac_f32_e32 v7, v72, v103
	v_fmac_f32_e32 v8, v72, v104
	v_fmac_f32_e32 v0, v73, v108
	v_fmac_f32_e32 v1, v73, v109
	v_fmac_f32_e32 v2, v73, v110
	v_fmac_f32_e32 v3, v73, v111
	v_fmac_f32_e32 v4, v73, v112
	v_fmac_f32_e32 v5, v73, v113
	v_fmac_f32_e32 v6, v73, v114
	v_fmac_f32_e32 v7, v73, v115
	v_fmac_f32_e32 v8, v73, v116
	ds_read_b128 v[96:99], v9 offset:6912
	ds_read_b128 v[100:103], v9 offset:6928
	ds_read_b32 v104, v9 offset:6944
	ds_read_b128 v[108:111], v9 offset:6976
	ds_read_b128 v[112:115], v9 offset:6992
	ds_read_b32 v116, v9 offset:7008
	s_waitcnt lgkmcnt(6)
	v_fmac_f32_e32 v0, v74, v120
	v_fmac_f32_e32 v1, v74, v121
	v_fmac_f32_e32 v2, v74, v122
	v_fmac_f32_e32 v3, v74, v123
	v_fmac_f32_e32 v4, v74, v124
	v_fmac_f32_e32 v5, v74, v125
	v_fmac_f32_e32 v6, v74, v126
	v_fmac_f32_e32 v7, v74, v127
	v_fmac_f32_e32 v8, v74, v128
	v_fmac_f32_e32 v0, v75, v132
	v_fmac_f32_e32 v1, v75, v133
	v_fmac_f32_e32 v2, v75, v134
	v_fmac_f32_e32 v3, v75, v135
	v_fmac_f32_e32 v4, v75, v136
	v_fmac_f32_e32 v5, v75, v137
	v_fmac_f32_e32 v6, v75, v138
	v_fmac_f32_e32 v7, v75, v139
	v_fmac_f32_e32 v8, v75, v140
	ds_read_b128 v[120:123], v9 offset:7040
	ds_read_b128 v[124:127], v9 offset:7056
	ds_read_b32 v128, v9 offset:7072
	ds_read_b128 v[132:135], v9 offset:7104
	ds_read_b128 v[136:139], v9 offset:7120
	ds_read_b32 v140, v9 offset:7136
	s_waitcnt lgkmcnt(6)
	v_fmac_f32_e32 v0, v76, v96
	v_fmac_f32_e32 v1, v76, v97
	v_fmac_f32_e32 v2, v76, v98
	v_fmac_f32_e32 v3, v76, v99
	v_fmac_f32_e32 v4, v76, v100
	v_fmac_f32_e32 v5, v76, v101
	v_fmac_f32_e32 v6, v76, v102
	v_fmac_f32_e32 v7, v76, v103
	v_fmac_f32_e32 v8, v76, v104
	v_fmac_f32_e32 v0, v77, v108
	v_fmac_f32_e32 v1, v77, v109
	v_fmac_f32_e32 v2, v77, v110
	v_fmac_f32_e32 v3, v77, v111
	v_fmac_f32_e32 v4, v77, v112
	v_fmac_f32_e32 v5, v77, v113
	v_fmac_f32_e32 v6, v77, v114
	v_fmac_f32_e32 v7, v77, v115
	v_fmac_f32_e32 v8, v77, v116
	ds_read_b128 v[96:99], v9 offset:7168
	ds_read_b128 v[100:103], v9 offset:7184
	ds_read_b32 v104, v9 offset:7200
	ds_read_b128 v[108:111], v9 offset:7232
	ds_read_b128 v[112:115], v9 offset:7248
	ds_read_b32 v116, v9 offset:7264
	s_waitcnt lgkmcnt(6)
	v_fmac_f32_e32 v0, v78, v120
	v_fmac_f32_e32 v1, v78, v121
	v_fmac_f32_e32 v2, v78, v122
	v_fmac_f32_e32 v3, v78, v123
	v_fmac_f32_e32 v4, v78, v124
	v_fmac_f32_e32 v5, v78, v125
	v_fmac_f32_e32 v6, v78, v126
	v_fmac_f32_e32 v7, v78, v127
	v_fmac_f32_e32 v8, v78, v128
	v_fmac_f32_e32 v0, v79, v132
	v_fmac_f32_e32 v1, v79, v133
	v_fmac_f32_e32 v2, v79, v134
	v_fmac_f32_e32 v3, v79, v135
	v_fmac_f32_e32 v4, v79, v136
	v_fmac_f32_e32 v5, v79, v137
	v_fmac_f32_e32 v6, v79, v138
	v_fmac_f32_e32 v7, v79, v139
	v_fmac_f32_e32 v8, v79, v140
	s_waitcnt vmcnt(0)
	ds_read_b128 v[120:123], v9 offset:7296
	ds_read_b128 v[124:127], v9 offset:7312
	ds_read_b32 v128, v9 offset:7328
	ds_read_b128 v[132:135], v9 offset:7360
	ds_read_b128 v[136:139], v9 offset:7376
	ds_read_b32 v140, v9 offset:7392
	s_waitcnt lgkmcnt(6)
	v_fmac_f32_e32 v0, v80, v96
	v_fmac_f32_e32 v1, v80, v97
	v_fmac_f32_e32 v2, v80, v98
	v_fmac_f32_e32 v3, v80, v99
	v_fmac_f32_e32 v4, v80, v100
	v_fmac_f32_e32 v5, v80, v101
	v_fmac_f32_e32 v6, v80, v102
	v_fmac_f32_e32 v7, v80, v103
	v_fmac_f32_e32 v8, v80, v104
	v_fmac_f32_e32 v0, v81, v108
	v_fmac_f32_e32 v1, v81, v109
	v_fmac_f32_e32 v2, v81, v110
	v_fmac_f32_e32 v3, v81, v111
	v_fmac_f32_e32 v4, v81, v112
	v_fmac_f32_e32 v5, v81, v113
	v_fmac_f32_e32 v6, v81, v114
	v_fmac_f32_e32 v7, v81, v115
	v_fmac_f32_e32 v8, v81, v116
	ds_read_b128 v[96:99], v9 offset:7424
	ds_read_b128 v[100:103], v9 offset:7440
	ds_read_b32 v104, v9 offset:7456
	ds_read_b128 v[108:111], v9 offset:7488
	ds_read_b128 v[112:115], v9 offset:7504
	ds_read_b32 v116, v9 offset:7520
	s_waitcnt lgkmcnt(6)
	v_fmac_f32_e32 v0, v82, v120
	v_fmac_f32_e32 v1, v82, v121
	v_fmac_f32_e32 v2, v82, v122
	v_fmac_f32_e32 v3, v82, v123
	v_fmac_f32_e32 v4, v82, v124
	v_fmac_f32_e32 v5, v82, v125
	v_fmac_f32_e32 v6, v82, v126
	v_fmac_f32_e32 v7, v82, v127
	v_fmac_f32_e32 v8, v82, v128
	v_fmac_f32_e32 v0, v83, v132
	v_fmac_f32_e32 v1, v83, v133
	v_fmac_f32_e32 v2, v83, v134
	v_fmac_f32_e32 v3, v83, v135
	v_fmac_f32_e32 v4, v83, v136
	v_fmac_f32_e32 v5, v83, v137
	v_fmac_f32_e32 v6, v83, v138
	v_fmac_f32_e32 v7, v83, v139
	v_fmac_f32_e32 v8, v83, v140
	ds_read_b128 v[120:123], v9 offset:7552
	ds_read_b128 v[124:127], v9 offset:7568
	ds_read_b32 v128, v9 offset:7584
	ds_read_b128 v[132:135], v9 offset:7616
	ds_read_b128 v[136:139], v9 offset:7632
	ds_read_b32 v140, v9 offset:7648
	s_waitcnt lgkmcnt(6)
	v_fmac_f32_e32 v0, v84, v96
	v_fmac_f32_e32 v1, v84, v97
	v_fmac_f32_e32 v2, v84, v98
	v_fmac_f32_e32 v3, v84, v99
	v_fmac_f32_e32 v4, v84, v100
	v_fmac_f32_e32 v5, v84, v101
	v_fmac_f32_e32 v6, v84, v102
	v_fmac_f32_e32 v7, v84, v103
	v_fmac_f32_e32 v8, v84, v104
	v_fmac_f32_e32 v0, v85, v108
	v_fmac_f32_e32 v1, v85, v109
	v_fmac_f32_e32 v2, v85, v110
	v_fmac_f32_e32 v3, v85, v111
	v_fmac_f32_e32 v4, v85, v112
	v_fmac_f32_e32 v5, v85, v113
	v_fmac_f32_e32 v6, v85, v114
	v_fmac_f32_e32 v7, v85, v115
	v_fmac_f32_e32 v8, v85, v116
	ds_read_b128 v[96:99], v9 offset:7680
	ds_read_b128 v[100:103], v9 offset:7696
	ds_read_b32 v104, v9 offset:7712
	ds_read_b128 v[108:111], v9 offset:7744
	ds_read_b128 v[112:115], v9 offset:7760
	ds_read_b32 v116, v9 offset:7776
	s_waitcnt lgkmcnt(6)
	v_fmac_f32_e32 v0, v86, v120
	v_fmac_f32_e32 v1, v86, v121
	v_fmac_f32_e32 v2, v86, v122
	v_fmac_f32_e32 v3, v86, v123
	v_fmac_f32_e32 v4, v86, v124
	v_fmac_f32_e32 v5, v86, v125
	v_fmac_f32_e32 v6, v86, v126
	v_fmac_f32_e32 v7, v86, v127
	v_fmac_f32_e32 v8, v86, v128
	v_fmac_f32_e32 v0, v87, v132
	v_fmac_f32_e32 v1, v87, v133
	v_fmac_f32_e32 v2, v87, v134
	v_fmac_f32_e32 v3, v87, v135
	v_fmac_f32_e32 v4, v87, v136
	v_fmac_f32_e32 v5, v87, v137
	v_fmac_f32_e32 v6, v87, v138
	v_fmac_f32_e32 v7, v87, v139
	v_fmac_f32_e32 v8, v87, v140
	ds_read_b128 v[120:123], v9 offset:7808
	ds_read_b128 v[124:127], v9 offset:7824
	ds_read_b32 v128, v9 offset:7840
	ds_read_b128 v[132:135], v9 offset:7872
	ds_read_b128 v[136:139], v9 offset:7888
	ds_read_b32 v140, v9 offset:7904
	s_waitcnt lgkmcnt(6)
	v_fmac_f32_e32 v0, v88, v96
	v_fmac_f32_e32 v1, v88, v97
	v_fmac_f32_e32 v2, v88, v98
	v_fmac_f32_e32 v3, v88, v99
	v_fmac_f32_e32 v4, v88, v100
	v_fmac_f32_e32 v5, v88, v101
	v_fmac_f32_e32 v6, v88, v102
	v_fmac_f32_e32 v7, v88, v103
	v_fmac_f32_e32 v8, v88, v104
	v_fmac_f32_e32 v0, v89, v108
	v_fmac_f32_e32 v1, v89, v109
	v_fmac_f32_e32 v2, v89, v110
	v_fmac_f32_e32 v3, v89, v111
	v_fmac_f32_e32 v4, v89, v112
	v_fmac_f32_e32 v5, v89, v113
	v_fmac_f32_e32 v6, v89, v114
	v_fmac_f32_e32 v7, v89, v115
	v_fmac_f32_e32 v8, v89, v116
	ds_read_b128 v[96:99], v9 offset:7936
	ds_read_b128 v[100:103], v9 offset:7952
	ds_read_b32 v104, v9 offset:7968
	ds_read_b128 v[108:111], v9 offset:8000
	ds_read_b128 v[112:115], v9 offset:8016
	ds_read_b32 v116, v9 offset:8032
	s_waitcnt lgkmcnt(6)
	v_fmac_f32_e32 v0, v90, v120
	v_fmac_f32_e32 v1, v90, v121
	v_fmac_f32_e32 v2, v90, v122
	v_fmac_f32_e32 v3, v90, v123
	v_fmac_f32_e32 v4, v90, v124
	v_fmac_f32_e32 v5, v90, v125
	v_fmac_f32_e32 v6, v90, v126
	v_fmac_f32_e32 v7, v90, v127
	v_fmac_f32_e32 v8, v90, v128
	v_fmac_f32_e32 v0, v91, v132
	v_fmac_f32_e32 v1, v91, v133
	v_fmac_f32_e32 v2, v91, v134
	v_fmac_f32_e32 v3, v91, v135
	v_fmac_f32_e32 v4, v91, v136
	v_fmac_f32_e32 v5, v91, v137
	v_fmac_f32_e32 v6, v91, v138
	v_fmac_f32_e32 v7, v91, v139
	v_fmac_f32_e32 v8, v91, v140
	ds_read_b128 v[120:123], v9 offset:8064
	ds_read_b128 v[124:127], v9 offset:8080
	ds_read_b32 v128, v9 offset:8096
	ds_read_b128 v[132:135], v9 offset:8128
	ds_read_b128 v[136:139], v9 offset:8144
	ds_read_b32 v140, v9 offset:8160
	s_waitcnt lgkmcnt(6)
	v_fmac_f32_e32 v0, v92, v96
	v_fmac_f32_e32 v1, v92, v97
	v_fmac_f32_e32 v2, v92, v98
	v_fmac_f32_e32 v3, v92, v99
	v_fmac_f32_e32 v4, v92, v100
	v_fmac_f32_e32 v5, v92, v101
	v_fmac_f32_e32 v6, v92, v102
	v_fmac_f32_e32 v7, v92, v103
	v_fmac_f32_e32 v8, v92, v104
	v_fmac_f32_e32 v0, v93, v108
	v_fmac_f32_e32 v1, v93, v109
	v_fmac_f32_e32 v2, v93, v110
	v_fmac_f32_e32 v3, v93, v111
	v_fmac_f32_e32 v4, v93, v112
	v_fmac_f32_e32 v5, v93, v113
	v_fmac_f32_e32 v6, v93, v114
	v_fmac_f32_e32 v7, v93, v115
	v_fmac_f32_e32 v8, v93, v116
	s_waitcnt lgkmcnt(0)
	v_fmac_f32_e32 v0, v94, v120
	v_fmac_f32_e32 v1, v94, v121
	v_fmac_f32_e32 v2, v94, v122
	v_fmac_f32_e32 v3, v94, v123
	v_fmac_f32_e32 v4, v94, v124
	v_fmac_f32_e32 v5, v94, v125
	v_fmac_f32_e32 v6, v94, v126
	v_fmac_f32_e32 v7, v94, v127
	v_fmac_f32_e32 v8, v94, v128
	v_fmac_f32_e32 v0, v95, v132
	v_fmac_f32_e32 v1, v95, v133
	v_fmac_f32_e32 v2, v95, v134
	v_fmac_f32_e32 v3, v95, v135
	v_fmac_f32_e32 v4, v95, v136
	v_fmac_f32_e32 v5, v95, v137
	v_fmac_f32_e32 v6, v95, v138
	v_fmac_f32_e32 v7, v95, v139
	v_fmac_f32_e32 v8, v95, v140
	s_barrier
	s_lshl_b32 s16, s22, 1
	s_add_i32 s16, s16, s23
	s_mul_i32 s16, s16, 9
	s_mul_hi_u32 s17, s16, 0x6000
	s_mul_i32 s16, s16, 0x6000
	s_add_u32 s28, s12, s16
	s_addc_u32 s29, s13, s17
	global_store_dword v30, v0, s[28:29]
	s_add_u32 s28, s28, 0x6000
	s_addc_u32 s29, s29, 0
	global_store_dword v30, v1, s[28:29]
	s_add_u32 s28, s28, 0x6000
	s_addc_u32 s29, s29, 0
	global_store_dword v30, v2, s[28:29]
	s_add_u32 s28, s28, 0x6000
	s_addc_u32 s29, s29, 0
	global_store_dword v30, v3, s[28:29]
	s_add_u32 s28, s28, 0x6000
	s_addc_u32 s29, s29, 0
	global_store_dword v30, v4, s[28:29]
	s_add_u32 s28, s28, 0x6000
	s_addc_u32 s29, s29, 0
	global_store_dword v30, v5, s[28:29]
	s_add_u32 s28, s28, 0x6000
	s_addc_u32 s29, s29, 0
	global_store_dword v30, v6, s[28:29]
	s_add_u32 s28, s28, 0x6000
	s_addc_u32 s29, s29, 0
	global_store_dword v30, v7, s[28:29]
	s_add_u32 s28, s28, 0x6000
	s_addc_u32 s29, s29, 0
	global_store_dword v30, v8, s[28:29]
	s_add_i32 s20, s20, s21
	s_cmpk_gt_i32 s20, 0x5ff
	s_cbranch_scc0 .LBB0_11
